# first K-iteration peeled with srcC=0 in in-proj/gate/Wo/down GEMM loops (accumulator zero-init removed); plus scan LDS batching, moe_tables/gmlp load batching, inline 0.5
# speedup vs baseline: 1.0142x; 1.0055x over previous
.LBB0_263:
	s_ashr_i32 s71, s70, 31
	s_lshl_b64 s[28:29], s[70:71], 19
	s_add_u32 s72, s18, s28
	s_addc_u32 s73, s19, s29
	s_and_b64 s[28:29], s[38:39], exec
	s_cselect_b32 s36, s73, s77
	s_cselect_b32 s37, s72, s76
	s_ashr_i32 s65, s64, 31
	s_lshl_b64 s[28:29], s[64:65], 19
	s_add_u32 s74, s2, s28
	s_addc_u32 s75, s12, s29
	s_and_b64 s[28:29], s[38:39], exec
	s_cselect_b32 s43, s75, s81
	s_cselect_b32 s50, s74, s80
	s_add_u32 s76, s76, 0x40080
	s_addc_u32 s77, s77, 0
	s_add_u32 s51, s80, 0x100
	s_addc_u32 s65, s81, 0
	s_mov_b32 s71, -2
.Lpeel_inproj:
	s_add_u32 s28, s76, 0xfffc0080
	s_addc_u32 s29, s77, -1
	s_add_i32 s30, 0, 0x10000
	s_cmp_eq_u32 s71, 12
	s_cselect_b32 s83, s36, s29
	s_cselect_b32 s82, s37, s28
	v_add_u32_e32 v112, s30, v153
	s_cselect_b32 s81, s43, s65
	s_cselect_b32 s80, s50, s51
	s_add_i32 s31, 0, 0x14000
	ds_read_b128 v[130:133], v112
	ds_read_b128 v[134:137], v112 offset:1024
	ds_read_b128 v[156:159], v112 offset:2048
	ds_read_b128 v[160:163], v112 offset:3072
	v_add_u32_e32 v112, s31, v153
	ds_read_b128 v[164:167], v112
	ds_read_b128 v[168:171], v112 offset:1024
	ds_read_b128 v[172:175], v112 offset:2048
	ds_read_b128 v[176:179], v112 offset:3072
	v_lshl_add_u64 v[150:151], s[76:77], 0, v[146:147]
	s_add_i32 m0, s26, 0xc000
	ds_read_b128 v[180:183], v154
	ds_read_b128 v[184:187], v154 offset:1024
	ds_read_b128 v[188:191], v154 offset:2048
	ds_read_b128 v[192:195], v154 offset:3072
	ds_read_b128 v[206:209], v154 offset:4096
	ds_read_b128 v[210:213], v154 offset:5120
	ds_read_b128 v[216:219], v154 offset:6144
	ds_read_b128 v[220:223], v154 offset:7168
	global_load_lds_dwordx4 v[150:151], off
	v_lshl_add_u64 v[150:151], s[76:77], 0, v[148:149]
	s_add_i32 m0, s26, 0xe000
	s_nop 0
	global_load_lds_dwordx4 v[150:151], off
	s_waitcnt vmcnt(8)
	s_waitcnt lgkmcnt(0)
	s_barrier
	s_setprio 1
	s_waitcnt lgkmcnt(0)
	v_mfma_f32_16x16x32_bf16 v[126:129], v[130:133], v[180:183], 0
	v_mfma_f32_16x16x32_bf16 v[122:125], v[156:159], v[180:183], 0
	v_mfma_f32_16x16x32_bf16 v[118:121], v[130:133], v[188:191], 0
	v_mfma_f32_16x16x32_bf16 v[114:117], v[156:159], v[188:191], 0
	v_mfma_f32_16x16x32_bf16 v[100:103], v[130:133], v[206:209], 0
	v_mfma_f32_16x16x32_bf16 v[96:99], v[156:159], v[206:209], 0
	v_mfma_f32_16x16x32_bf16 v[84:87], v[130:133], v[216:219], 0
	v_mfma_f32_16x16x32_bf16 v[80:83], v[156:159], v[216:219], 0
	v_mfma_f32_16x16x32_bf16 v[126:129], v[134:137], v[184:187], v[126:129]
	v_mfma_f32_16x16x32_bf16 v[122:125], v[160:163], v[184:187], v[122:125]
	v_mfma_f32_16x16x32_bf16 v[118:121], v[134:137], v[192:195], v[118:121]
	v_mfma_f32_16x16x32_bf16 v[114:117], v[160:163], v[192:195], v[114:117]
	v_mfma_f32_16x16x32_bf16 v[100:103], v[134:137], v[210:213], v[100:103]
	v_mfma_f32_16x16x32_bf16 v[96:99], v[160:163], v[210:213], v[96:99]
	v_mfma_f32_16x16x32_bf16 v[84:87], v[134:137], v[220:223], v[84:87]
	v_mfma_f32_16x16x32_bf16 v[80:83], v[160:163], v[220:223], v[80:83]
	s_setprio 0
	s_setprio 1
	v_mfma_f32_16x16x32_bf16 v[108:111], v[164:167], v[180:183], 0
	v_mfma_f32_16x16x32_bf16 v[104:107], v[172:175], v[180:183], 0
	v_mfma_f32_16x16x32_bf16 v[92:95], v[164:167], v[188:191], 0
	v_mfma_f32_16x16x32_bf16 v[88:91], v[172:175], v[188:191], 0
	v_mfma_f32_16x16x32_bf16 v[76:79], v[164:167], v[206:209], 0
	v_mfma_f32_16x16x32_bf16 v[72:75], v[172:175], v[206:209], 0
	v_mfma_f32_16x16x32_bf16 v[68:71], v[164:167], v[216:219], 0
	v_mfma_f32_16x16x32_bf16 v[64:67], v[172:175], v[216:219], 0
	v_mfma_f32_16x16x32_bf16 v[108:111], v[168:171], v[184:187], v[108:111]
	v_mfma_f32_16x16x32_bf16 v[104:107], v[176:179], v[184:187], v[104:107]
	v_mfma_f32_16x16x32_bf16 v[92:95], v[168:171], v[192:195], v[92:95]
	v_mfma_f32_16x16x32_bf16 v[88:91], v[176:179], v[192:195], v[88:91]
	v_mfma_f32_16x16x32_bf16 v[76:79], v[168:171], v[210:213], v[76:79]
	v_mfma_f32_16x16x32_bf16 v[72:75], v[176:179], v[210:213], v[72:75]
	v_mfma_f32_16x16x32_bf16 v[68:71], v[168:171], v[220:223], v[68:71]
	v_mfma_f32_16x16x32_bf16 v[64:67], v[176:179], v[220:223], v[64:67]
	s_setprio 0
	s_barrier
	s_add_i32 s28, s30, s13
	v_lshl_add_u64 v[150:151], s[80:81], 0, v[140:141]
	s_mov_b32 m0, s28
	ds_read_b128 v[180:183], v154 offset:16384
	ds_read_b128 v[184:187], v154 offset:17408
	ds_read_b128 v[188:191], v154 offset:18432
	ds_read_b128 v[192:195], v154 offset:19456
	ds_read_b128 v[206:209], v154 offset:20480
	ds_read_b128 v[210:213], v154 offset:21504
	ds_read_b128 v[216:219], v154 offset:22528
	ds_read_b128 v[220:223], v154 offset:23552
	global_load_lds_dwordx4 v[150:151], off
	s_add_i32 m0, s28, 0x2000
	s_add_u32 s28, s80, 0x40000
	v_lshl_add_u64 v[224:225], s[80:81], 0, v[144:145]
	s_addc_u32 s29, s81, 0
	s_add_i32 s30, s31, s13
	global_load_lds_dwordx4 v[224:225], off
	v_lshl_add_u64 v[226:227], s[28:29], 0, v[140:141]
	s_mov_b32 m0, s30
	v_lshl_add_u64 v[228:229], s[82:83], 0, v[142:143]
	global_load_lds_dwordx4 v[226:227], off
	v_lshl_add_u64 v[226:227], s[28:29], 0, v[144:145]
	s_add_i32 m0, s30, 0x2000
	s_nop 0
	global_load_lds_dwordx4 v[226:227], off
	v_lshl_add_u64 v[226:227], s[82:83], 0, v[138:139]
	s_mov_b32 m0, s26
	s_nop 0
	global_load_lds_dwordx4 v[226:227], off
	s_mov_b32 m0, s27
	s_nop 0
	global_load_lds_dwordx4 v[228:229], off
	s_waitcnt vmcnt(8)
	s_waitcnt lgkmcnt(0)
	s_barrier
	s_setprio 1
	s_waitcnt lgkmcnt(0)
	v_mfma_f32_16x16x32_bf16 v[60:63], v[130:133], v[180:183], 0
	v_mfma_f32_16x16x32_bf16 v[56:59], v[156:159], v[180:183], 0
	v_mfma_f32_16x16x32_bf16 v[52:55], v[130:133], v[188:191], 0
	v_mfma_f32_16x16x32_bf16 v[48:51], v[156:159], v[188:191], 0
	v_mfma_f32_16x16x32_bf16 v[36:39], v[130:133], v[206:209], 0
	v_mfma_f32_16x16x32_bf16 v[32:35], v[156:159], v[206:209], 0
	v_mfma_f32_16x16x32_bf16 v[20:23], v[130:133], v[216:219], 0
	v_mfma_f32_16x16x32_bf16 v[16:19], v[156:159], v[216:219], 0
	v_mfma_f32_16x16x32_bf16 v[60:63], v[134:137], v[184:187], v[60:63]
	v_mfma_f32_16x16x32_bf16 v[56:59], v[160:163], v[184:187], v[56:59]
	v_mfma_f32_16x16x32_bf16 v[52:55], v[134:137], v[192:195], v[52:55]
	v_mfma_f32_16x16x32_bf16 v[48:51], v[160:163], v[192:195], v[48:51]
	v_mfma_f32_16x16x32_bf16 v[36:39], v[134:137], v[210:213], v[36:39]
	v_mfma_f32_16x16x32_bf16 v[32:35], v[160:163], v[210:213], v[32:35]
	v_mfma_f32_16x16x32_bf16 v[20:23], v[134:137], v[220:223], v[20:23]
	v_mfma_f32_16x16x32_bf16 v[16:19], v[160:163], v[220:223], v[16:19]
	s_setprio 0
	s_setprio 1
	v_mfma_f32_16x16x32_bf16 v[44:47], v[164:167], v[180:183], 0
	v_mfma_f32_16x16x32_bf16 v[40:43], v[172:175], v[180:183], 0
	v_mfma_f32_16x16x32_bf16 v[28:31], v[164:167], v[188:191], 0
	v_mfma_f32_16x16x32_bf16 v[24:27], v[172:175], v[188:191], 0
	v_mfma_f32_16x16x32_bf16 v[12:15], v[164:167], v[206:209], 0
	v_mfma_f32_16x16x32_bf16 v[8:11], v[172:175], v[206:209], 0
	v_mfma_f32_16x16x32_bf16 v[4:7], v[164:167], v[216:219], 0
	v_mfma_f32_16x16x32_bf16 v[0:3], v[172:175], v[216:219], 0
	v_mfma_f32_16x16x32_bf16 v[44:47], v[168:171], v[184:187], v[44:47]
	v_mfma_f32_16x16x32_bf16 v[40:43], v[176:179], v[184:187], v[40:43]
	v_mfma_f32_16x16x32_bf16 v[28:31], v[168:171], v[192:195], v[28:31]
	v_mfma_f32_16x16x32_bf16 v[24:27], v[176:179], v[192:195], v[24:27]
	v_mfma_f32_16x16x32_bf16 v[12:15], v[168:171], v[210:213], v[12:15]
	v_mfma_f32_16x16x32_bf16 v[8:11], v[176:179], v[210:213], v[8:11]
	v_mfma_f32_16x16x32_bf16 v[4:7], v[168:171], v[220:223], v[4:7]
	v_mfma_f32_16x16x32_bf16 v[0:3], v[176:179], v[220:223], v[0:3]
	s_setprio 0
	s_barrier
	s_add_i32 s30, 0, 0x18000
	v_add_u32_e32 v112, s30, v153
	s_add_i32 s31, 0, 0x1c000
	ds_read_b128 v[130:133], v112
	ds_read_b128 v[134:137], v112 offset:1024
	ds_read_b128 v[156:159], v112 offset:2048
	ds_read_b128 v[160:163], v112 offset:3072
	v_add_u32_e32 v112, s31, v153
	ds_read_b128 v[164:167], v112
	ds_read_b128 v[168:171], v112 offset:1024
	ds_read_b128 v[172:175], v112 offset:2048
	ds_read_b128 v[176:179], v112 offset:3072
	s_add_u32 s28, s82, 0x40000
	s_addc_u32 s29, s83, 0
	s_mov_b32 m0, s34
	v_lshl_add_u64 v[230:231], s[28:29], 0, v[138:139]
	ds_read_b128 v[180:183], v154 offset:32768
	ds_read_b128 v[184:187], v154 offset:33792
	ds_read_b128 v[188:191], v154 offset:34816
	ds_read_b128 v[192:195], v154 offset:35840
	ds_read_b128 v[206:209], v154 offset:36864
	ds_read_b128 v[210:213], v154 offset:37888
	ds_read_b128 v[216:219], v154 offset:38912
	ds_read_b128 v[220:223], v154 offset:39936
	global_load_lds_dwordx4 v[230:231], off
	v_lshl_add_u64 v[230:231], s[28:29], 0, v[142:143]
	s_mov_b32 m0, s14
	s_nop 0
	global_load_lds_dwordx4 v[230:231], off
	s_waitcnt vmcnt(8)
	s_waitcnt lgkmcnt(0)
	s_barrier
	s_setprio 1
	s_waitcnt lgkmcnt(0)
	v_mfma_f32_16x16x32_bf16 v[126:129], v[130:133], v[180:183], v[126:129]
	v_mfma_f32_16x16x32_bf16 v[122:125], v[156:159], v[180:183], v[122:125]
	v_mfma_f32_16x16x32_bf16 v[118:121], v[130:133], v[188:191], v[118:121]
	v_mfma_f32_16x16x32_bf16 v[114:117], v[156:159], v[188:191], v[114:117]
	v_mfma_f32_16x16x32_bf16 v[100:103], v[130:133], v[206:209], v[100:103]
	v_mfma_f32_16x16x32_bf16 v[96:99], v[156:159], v[206:209], v[96:99]
	v_mfma_f32_16x16x32_bf16 v[84:87], v[130:133], v[216:219], v[84:87]
	v_mfma_f32_16x16x32_bf16 v[80:83], v[156:159], v[216:219], v[80:83]
	v_mfma_f32_16x16x32_bf16 v[126:129], v[134:137], v[184:187], v[126:129]
	v_mfma_f32_16x16x32_bf16 v[122:125], v[160:163], v[184:187], v[122:125]
	v_mfma_f32_16x16x32_bf16 v[118:121], v[134:137], v[192:195], v[118:121]
	v_mfma_f32_16x16x32_bf16 v[114:117], v[160:163], v[192:195], v[114:117]
	v_mfma_f32_16x16x32_bf16 v[100:103], v[134:137], v[210:213], v[100:103]
	v_mfma_f32_16x16x32_bf16 v[96:99], v[160:163], v[210:213], v[96:99]
	v_mfma_f32_16x16x32_bf16 v[84:87], v[134:137], v[220:223], v[84:87]
	v_mfma_f32_16x16x32_bf16 v[80:83], v[160:163], v[220:223], v[80:83]
	s_setprio 0
	s_setprio 1
	v_mfma_f32_16x16x32_bf16 v[108:111], v[164:167], v[180:183], v[108:111]
	v_mfma_f32_16x16x32_bf16 v[104:107], v[172:175], v[180:183], v[104:107]
	v_mfma_f32_16x16x32_bf16 v[92:95], v[164:167], v[188:191], v[92:95]
	v_mfma_f32_16x16x32_bf16 v[88:91], v[172:175], v[188:191], v[88:91]
	v_mfma_f32_16x16x32_bf16 v[76:79], v[164:167], v[206:209], v[76:79]
	v_mfma_f32_16x16x32_bf16 v[72:75], v[172:175], v[206:209], v[72:75]
	v_mfma_f32_16x16x32_bf16 v[68:71], v[164:167], v[216:219], v[68:71]
	v_mfma_f32_16x16x32_bf16 v[64:67], v[172:175], v[216:219], v[64:67]
	v_mfma_f32_16x16x32_bf16 v[108:111], v[168:171], v[184:187], v[108:111]
	v_mfma_f32_16x16x32_bf16 v[104:107], v[176:179], v[184:187], v[104:107]
	v_mfma_f32_16x16x32_bf16 v[92:95], v[168:171], v[192:195], v[92:95]
	v_mfma_f32_16x16x32_bf16 v[88:91], v[176:179], v[192:195], v[88:91]
	v_mfma_f32_16x16x32_bf16 v[76:79], v[168:171], v[210:213], v[76:79]
	v_mfma_f32_16x16x32_bf16 v[72:75], v[176:179], v[210:213], v[72:75]
	v_mfma_f32_16x16x32_bf16 v[68:71], v[168:171], v[220:223], v[68:71]
	v_mfma_f32_16x16x32_bf16 v[64:67], v[176:179], v[220:223], v[64:67]
	s_setprio 0
	s_barrier
	s_add_i32 s28, s30, s13
	v_lshl_add_u64 v[150:151], v[150:151], 0, s[56:57]
	s_mov_b32 m0, s28
	ds_read_b128 v[180:183], v154 offset:49152
	ds_read_b128 v[184:187], v154 offset:50176
	ds_read_b128 v[188:191], v154 offset:51200
	ds_read_b128 v[192:195], v154 offset:52224
	ds_read_b128 v[206:209], v154 offset:53248
	ds_read_b128 v[210:213], v154 offset:54272
	ds_read_b128 v[216:219], v154 offset:55296
	ds_read_b128 v[220:223], v154 offset:56320
	global_load_lds_dwordx4 v[150:151], off
	s_add_i32 m0, s28, 0x2000
	s_add_u32 s28, s80, 0x40080
	v_lshl_add_u64 v[150:151], v[224:225], 0, s[56:57]
	s_addc_u32 s29, s81, 0
	s_add_i32 s30, s31, s13
	global_load_lds_dwordx4 v[150:151], off
	v_lshl_add_u64 v[150:151], s[28:29], 0, v[140:141]
	s_mov_b32 m0, s30
	s_nop 0
	global_load_lds_dwordx4 v[150:151], off
	v_lshl_add_u64 v[150:151], s[28:29], 0, v[144:145]
	s_add_i32 m0, s30, 0x2000
	s_nop 0
	global_load_lds_dwordx4 v[150:151], off
	v_lshl_add_u64 v[150:151], v[226:227], 0, s[56:57]
	s_mov_b32 m0, s33
	s_nop 0
	global_load_lds_dwordx4 v[150:151], off
	v_lshl_add_u64 v[150:151], v[228:229], 0, s[56:57]
	s_mov_b32 m0, s69
	s_nop 0
	global_load_lds_dwordx4 v[150:151], off
	s_waitcnt vmcnt(8)
	s_waitcnt lgkmcnt(0)
	s_barrier
	s_setprio 1
	s_waitcnt lgkmcnt(0)
	v_mfma_f32_16x16x32_bf16 v[60:63], v[130:133], v[180:183], v[60:63]
	v_mfma_f32_16x16x32_bf16 v[56:59], v[156:159], v[180:183], v[56:59]
	v_mfma_f32_16x16x32_bf16 v[52:55], v[130:133], v[188:191], v[52:55]
	v_mfma_f32_16x16x32_bf16 v[48:51], v[156:159], v[188:191], v[48:51]
	v_mfma_f32_16x16x32_bf16 v[36:39], v[130:133], v[206:209], v[36:39]
	v_mfma_f32_16x16x32_bf16 v[32:35], v[156:159], v[206:209], v[32:35]
	v_mfma_f32_16x16x32_bf16 v[20:23], v[130:133], v[216:219], v[20:23]
	v_mfma_f32_16x16x32_bf16 v[16:19], v[156:159], v[216:219], v[16:19]
	v_mfma_f32_16x16x32_bf16 v[60:63], v[134:137], v[184:187], v[60:63]
	v_mfma_f32_16x16x32_bf16 v[56:59], v[160:163], v[184:187], v[56:59]
	v_mfma_f32_16x16x32_bf16 v[52:55], v[134:137], v[192:195], v[52:55]
	v_mfma_f32_16x16x32_bf16 v[48:51], v[160:163], v[192:195], v[48:51]
	v_mfma_f32_16x16x32_bf16 v[36:39], v[134:137], v[210:213], v[36:39]
	v_mfma_f32_16x16x32_bf16 v[32:35], v[160:163], v[210:213], v[32:35]
	v_mfma_f32_16x16x32_bf16 v[20:23], v[134:137], v[220:223], v[20:23]
	v_mfma_f32_16x16x32_bf16 v[16:19], v[160:163], v[220:223], v[16:19]
	s_setprio 0
	s_setprio 1
	v_mfma_f32_16x16x32_bf16 v[44:47], v[164:167], v[180:183], v[44:47]
	v_mfma_f32_16x16x32_bf16 v[40:43], v[172:175], v[180:183], v[40:43]
	v_mfma_f32_16x16x32_bf16 v[28:31], v[164:167], v[188:191], v[28:31]
	v_mfma_f32_16x16x32_bf16 v[24:27], v[172:175], v[188:191], v[24:27]
	v_mfma_f32_16x16x32_bf16 v[12:15], v[164:167], v[206:209], v[12:15]
	v_mfma_f32_16x16x32_bf16 v[8:11], v[172:175], v[206:209], v[8:11]
	v_mfma_f32_16x16x32_bf16 v[4:7], v[164:167], v[216:219], v[4:7]
	v_mfma_f32_16x16x32_bf16 v[0:3], v[172:175], v[216:219], v[0:3]
	v_mfma_f32_16x16x32_bf16 v[44:47], v[168:171], v[184:187], v[44:47]
	v_mfma_f32_16x16x32_bf16 v[40:43], v[176:179], v[184:187], v[40:43]
	v_mfma_f32_16x16x32_bf16 v[28:31], v[168:171], v[192:195], v[28:31]
	v_mfma_f32_16x16x32_bf16 v[24:27], v[176:179], v[192:195], v[24:27]
	v_mfma_f32_16x16x32_bf16 v[12:15], v[168:171], v[210:213], v[12:15]
	v_mfma_f32_16x16x32_bf16 v[8:11], v[176:179], v[210:213], v[8:11]
	v_mfma_f32_16x16x32_bf16 v[4:7], v[168:171], v[220:223], v[4:7]
	v_mfma_f32_16x16x32_bf16 v[0:3], v[176:179], v[220:223], v[0:3]
	s_setprio 0
	s_barrier
	s_add_i32 s71, s71, 2
	s_add_u32 s76, s76, 0x100
	s_addc_u32 s77, s77, 0
	s_add_u32 s51, s51, 0x100
	s_addc_u32 s65, s65, 0
	s_cmp_gt_u32 s71, 13

.LBB0_607:
	s_and_b32 s28, s28, 0x10000
	v_add_u32_e32 v65, s28, v61
	ds_read_b128 v[70:73], v65
	ds_read_b128 v[74:77], v65 offset:1024
	ds_read_b128 v[78:81], v65 offset:2048
	ds_read_b128 v[82:85], v65 offset:3072
	ds_read_b128 v[86:89], v65 offset:4096
	ds_read_b128 v[90:93], v65 offset:5120
	ds_read_b128 v[94:97], v65 offset:6144
	ds_read_b128 v[98:101], v65 offset:7168
	ds_read_b128 v[118:121], v65 offset:8192
	ds_read_b128 v[122:125], v65 offset:9216
	ds_read_b128 v[126:129], v65 offset:10240
	ds_read_b128 v[130:133], v65 offset:11264
	ds_read_b128 v[134:137], v65 offset:12288
	ds_read_b128 v[138:141], v65 offset:13312
	ds_read_b128 v[142:145], v65 offset:14336
	s_cmp_lt_u32 s49, 4
	s_movk_i32 s28, 0x11ff
	s_cselect_b32 s28, 0xff, s28
	s_add_i32 s49, s49, 1
	v_cvt_pk_bf16_f32 v20, v0, v1
	v_cvt_pk_bf16_f32 v21, v2, v3
	v_cvt_pk_bf16_f32 v22, v4, v5
	v_cvt_pk_bf16_f32 v23, v6, v7
	v_lshlrev_b32_e32 v32, 16, v28
	v_and_b32_e32 v33, 0xffff0000, v28
	v_lshlrev_b32_e32 v34, 16, v29
	v_and_b32_e32 v35, 0xffff0000, v29
	v_cvt_pk_bf16_f32 v16, v8, v9
	v_cvt_pk_bf16_f32 v17, v10, v11
	v_cvt_pk_bf16_f32 v18, v12, v13
	v_cvt_pk_bf16_f32 v19, v14, v15
	v_lshlrev_b32_e32 v28, 16, v30
	v_and_b32_e32 v29, 0xffff0000, v30
	v_lshlrev_b32_e32 v30, 16, v31
	v_and_b32_e32 v31, 0xffff0000, v31
	v_lshlrev_b32_e32 v36, 16, v24
	v_and_b32_e32 v37, 0xffff0000, v24
	v_lshlrev_b32_e32 v38, 16, v25
	v_and_b32_e32 v39, 0xffff0000, v25
	v_lshlrev_b32_e32 v24, 16, v26
	v_and_b32_e32 v25, 0xffff0000, v26
	v_lshlrev_b32_e32 v26, 16, v27
	v_and_b32_e32 v27, 0xffff0000, v27
	s_waitcnt lgkmcnt(7)
	s_nop 1
	v_mfma_f32_16x16x32_bf16 v[32:35], v[70:73], v[20:23], v[32:35]
	v_mfma_f32_16x16x32_bf16 v[28:31], v[78:81], v[20:23], v[28:31]
	v_mfma_f32_16x16x32_bf16 v[36:39], v[86:89], v[20:23], v[36:39]
	v_mfma_f32_16x16x32_bf16 v[24:27], v[94:97], v[20:23], v[24:27]
	v_mfma_f32_16x16x32_bf16 v[32:35], v[74:77], v[16:19], v[32:35]
	v_mfma_f32_16x16x32_bf16 v[40:43], v[82:85], v[16:19], v[28:31]
	v_mfma_f32_16x16x32_bf16 v[36:39], v[90:93], v[16:19], v[36:39]
	v_mfma_f32_16x16x32_bf16 v[66:69], v[98:101], v[16:19], v[24:27]
	s_waitcnt lgkmcnt(0)
	ds_read_b128 v[146:149], v65 offset:15360
	ds_read_b128 v[102:105], v65 offset:16384
	ds_read_b128 v[106:109], v65 offset:17408
	ds_read_b128 v[150:153], v65 offset:18432
	ds_read_b128 v[154:157], v65 offset:19456
	ds_read_b128 v[158:161], v65 offset:20480
	ds_read_b128 v[162:165], v65 offset:21504
	ds_read_b128 v[206:209], v65 offset:22528
	ds_read_b128 v[210:213], v65 offset:23552
	ds_read_b128 v[226:229], v65 offset:24576
	ds_read_b128 v[230:233], v65 offset:25600
	ds_read_b128 v[234:237], v65 offset:26624
	ds_read_b128 v[238:241], v65 offset:27648
	ds_read_b128 v[242:245], v65 offset:28672
	v_pk_mul_f32 v[2:3], v[2:3], v[58:59] op_sel_hi:[1,0]
	v_pk_mul_f32 v[0:1], v[0:1], v[58:59] op_sel_hi:[1,0]
	v_pk_mul_f32 v[6:7], v[6:7], v[58:59] op_sel_hi:[1,0]
	v_pk_mul_f32 v[4:5], v[4:5], v[58:59] op_sel_hi:[1,0]
	v_pk_mul_f32 v[10:11], v[10:11], v[58:59] op_sel_hi:[1,0]
	v_pk_mul_f32 v[8:9], v[8:9], v[58:59] op_sel_hi:[1,0]
	v_pk_mul_f32 v[14:15], v[14:15], v[58:59] op_sel_hi:[1,0]
	v_pk_mul_f32 v[12:13], v[12:13], v[58:59] op_sel_hi:[1,0]
	v_cvt_pk_bf16_f32 v28, v32, v33
	v_cvt_pk_bf16_f32 v29, v34, v35
	v_cvt_pk_bf16_f32 v30, v40, v41
	v_cvt_pk_bf16_f32 v31, v42, v43
	v_cvt_pk_bf16_f32 v24, v36, v37
	v_cvt_pk_bf16_f32 v25, v38, v39
	v_cvt_pk_bf16_f32 v26, v66, v67
	v_cvt_pk_bf16_f32 v27, v68, v69
	s_waitcnt lgkmcnt(0)
	ds_read_b128 v[70:73], v65 offset:29696
	ds_read_b128 v[74:77], v65 offset:30720
	ds_read_b128 v[78:81], v65 offset:31744
	s_nop 0
	v_mfma_f32_16x16x32_bf16 v[32:35], v[118:121], v[20:23], 0
	v_mfma_f32_16x16x32_bf16 v[40:43], v[126:129], v[20:23], 0
	v_mfma_f32_16x16x32_bf16 v[32:35], v[102:105], v[28:31], v[32:35]
	v_mfma_f32_16x16x32_bf16 v[40:43], v[150:153], v[28:31], v[40:43]
	v_mfma_f32_16x16x32_bf16 v[32:35], v[122:125], v[16:19], v[32:35]
	v_mfma_f32_16x16x32_bf16 v[40:43], v[130:133], v[16:19], v[40:43]
	v_mfma_f32_16x16x32_bf16 v[36:39], v[106:109], v[24:27], v[32:35]
	v_mfma_f32_16x16x32_bf16 v[40:43], v[154:157], v[24:27], v[40:43]
	v_mfma_f32_16x16x32_bf16 v[32:35], v[134:137], v[20:23], 0
	v_mfma_f32_16x16x32_bf16 v[32:35], v[158:161], v[28:31], v[32:35]
	v_mfma_f32_16x16x32_bf16 v[32:35], v[138:141], v[16:19], v[32:35]
	v_mfma_f32_16x16x32_bf16 v[32:35], v[162:165], v[24:27], v[32:35]
	v_mfma_f32_16x16x32_bf16 v[20:23], v[142:145], v[20:23], 0
	v_mfma_f32_16x16x32_bf16 v[20:23], v[206:209], v[28:31], v[20:23]
	v_mfma_f32_16x16x32_bf16 v[16:19], v[146:149], v[16:19], v[20:23]
	v_mfma_f32_16x16x32_bf16 v[16:19], v[210:213], v[24:27], v[16:19]
	s_waitcnt lgkmcnt(0)
	v_mfma_f32_16x16x32_bf16 v[0:3], v[226:229], v[28:31], v[0:3]
	v_mfma_f32_16x16x32_bf16 v[4:7], v[234:237], v[28:31], v[4:7]
	v_mfma_f32_16x16x32_bf16 v[8:11], v[242:245], v[28:31], v[8:11]
	v_mfma_f32_16x16x32_bf16 v[12:15], v[74:77], v[28:31], v[12:15]
	v_mfma_f32_16x16x32_bf16 v[0:3], v[230:233], v[24:27], v[0:3]
	v_mfma_f32_16x16x32_bf16 v[4:7], v[238:241], v[24:27], v[4:7]
	v_mfma_f32_16x16x32_bf16 v[8:11], v[70:73], v[24:27], v[8:11]
	v_mfma_f32_16x16x32_bf16 v[12:15], v[78:81], v[24:27], v[12:15]
	v_cvt_pk_bf16_f32 v16, v16, s0
	v_cvt_pk_bf16_f32 v18, v18, s0
	v_add_u32_e32 v24, s28, v64
	v_add_u32_e32 v22, s48, v60
	v_add_u32_e32 v20, 51, v24
	v_cndmask_b32_e64 v20, v20, v22, s[38:39]
	v_ashrrev_i32_e32 v21, 31, v20
	v_lshl_add_u64 v[20:21], s[6:7], 0, v[20:21]
	v_lshlrev_b64 v[20:21], 9, v[20:21]
	v_cvt_pk_bf16_f32 v23, v36, s0
	v_lshl_add_u64 v[20:21], v[48:49], 0, v[20:21]
	global_store_short v[20:21], v23, off
	v_add_u32_e32 v20, 1, v22
	v_add_u32_e32 v21, 50, v24
	v_cndmask_b32_e64 v20, v21, v20, s[38:39]
	v_ashrrev_i32_e32 v21, 31, v20
	v_lshl_add_u64 v[20:21], s[6:7], 0, v[20:21]
	v_lshlrev_b64 v[20:21], 9, v[20:21]
	v_cvt_pk_bf16_f32 v23, v37, s0
	v_lshl_add_u64 v[20:21], v[48:49], 0, v[20:21]
	global_store_short v[20:21], v23, off
	v_add_u32_e32 v20, 2, v22
	v_add_u32_e32 v21, 49, v24
	v_cndmask_b32_e64 v20, v21, v20, s[38:39]
	v_ashrrev_i32_e32 v21, 31, v20
	v_lshl_add_u64 v[20:21], s[6:7], 0, v[20:21]
	v_lshlrev_b64 v[20:21], 9, v[20:21]
	v_cvt_pk_bf16_f32 v23, v38, s0
	v_lshl_add_u64 v[20:21], v[48:49], 0, v[20:21]
	global_store_short v[20:21], v23, off
	v_add_u32_e32 v20, 3, v22
	v_add_u32_e32 v21, 48, v24
	v_cndmask_b32_e64 v20, v21, v20, s[38:39]
	v_ashrrev_i32_e32 v21, 31, v20
	v_lshl_add_u64 v[20:21], s[6:7], 0, v[20:21]
	v_lshlrev_b64 v[20:21], 9, v[20:21]
	v_cvt_pk_bf16_f32 v23, v39, s0
	v_lshl_add_u64 v[20:21], v[48:49], 0, v[20:21]
	global_store_short v[20:21], v23, off
	v_add_u32_e32 v20, 16, v22
	v_add_u32_e32 v21, 35, v24
	v_cndmask_b32_e64 v20, v21, v20, s[38:39]
	v_ashrrev_i32_e32 v21, 31, v20
	v_lshl_add_u64 v[20:21], s[6:7], 0, v[20:21]
	v_lshlrev_b64 v[20:21], 9, v[20:21]
	v_cvt_pk_bf16_f32 v23, v40, s0
	v_lshl_add_u64 v[20:21], v[48:49], 0, v[20:21]
	global_store_short v[20:21], v23, off
	v_add_u32_e32 v20, 17, v22
	v_add_u32_e32 v21, 34, v24
	v_cndmask_b32_e64 v20, v21, v20, s[38:39]
	v_ashrrev_i32_e32 v21, 31, v20
	v_lshl_add_u64 v[20:21], s[6:7], 0, v[20:21]
	v_lshlrev_b64 v[20:21], 9, v[20:21]
	v_cvt_pk_bf16_f32 v23, v41, s0
	v_lshl_add_u64 v[20:21], v[48:49], 0, v[20:21]
	global_store_short v[20:21], v23, off
	v_add_u32_e32 v20, 18, v22
	v_add_u32_e32 v21, 33, v24
	v_cndmask_b32_e64 v20, v21, v20, s[38:39]
	v_ashrrev_i32_e32 v21, 31, v20
	v_lshl_add_u64 v[20:21], s[6:7], 0, v[20:21]
	v_lshlrev_b64 v[20:21], 9, v[20:21]
	v_cvt_pk_bf16_f32 v23, v42, s0
	v_lshl_add_u64 v[20:21], v[48:49], 0, v[20:21]
	global_store_short v[20:21], v23, off
	v_add_u32_e32 v20, 19, v22
	v_add_u32_e32 v21, 32, v24
	v_cndmask_b32_e64 v20, v21, v20, s[38:39]
	v_ashrrev_i32_e32 v21, 31, v20
	v_lshl_add_u64 v[20:21], s[6:7], 0, v[20:21]
	v_lshlrev_b64 v[20:21], 9, v[20:21]
	v_cvt_pk_bf16_f32 v23, v43, s0
	v_lshl_add_u64 v[20:21], v[48:49], 0, v[20:21]
	global_store_short v[20:21], v23, off
	v_add_u32_e32 v20, 32, v22
	v_add_u32_e32 v21, 19, v24
	v_cndmask_b32_e64 v20, v21, v20, s[38:39]
	v_ashrrev_i32_e32 v21, 31, v20
	v_lshl_add_u64 v[20:21], s[6:7], 0, v[20:21]
	v_lshlrev_b64 v[20:21], 9, v[20:21]
	v_cvt_pk_bf16_f32 v23, v32, s0
	v_lshl_add_u64 v[20:21], v[48:49], 0, v[20:21]
	global_store_short v[20:21], v23, off
	v_add_u32_e32 v20, 33, v22
	v_add_u32_e32 v21, 18, v24
	v_cndmask_b32_e64 v20, v21, v20, s[38:39]
	v_ashrrev_i32_e32 v21, 31, v20
	v_lshl_add_u64 v[20:21], s[6:7], 0, v[20:21]
	v_lshlrev_b64 v[20:21], 9, v[20:21]
	v_cvt_pk_bf16_f32 v23, v33, s0
	v_lshl_add_u64 v[20:21], v[48:49], 0, v[20:21]
	global_store_short v[20:21], v23, off
	v_add_u32_e32 v20, 34, v22
	v_add_u32_e32 v21, 17, v24
	v_cndmask_b32_e64 v20, v21, v20, s[38:39]
	v_ashrrev_i32_e32 v21, 31, v20
	v_lshl_add_u64 v[20:21], s[6:7], 0, v[20:21]
	v_lshlrev_b64 v[20:21], 9, v[20:21]
	v_cvt_pk_bf16_f32 v23, v34, s0
	v_lshl_add_u64 v[20:21], v[48:49], 0, v[20:21]
	global_store_short v[20:21], v23, off
	v_add_u32_e32 v20, 35, v22
	v_add_u32_e32 v21, 16, v24
	v_cndmask_b32_e64 v20, v21, v20, s[38:39]
	v_ashrrev_i32_e32 v21, 31, v20
	v_lshl_add_u64 v[20:21], s[6:7], 0, v[20:21]
	v_lshlrev_b64 v[20:21], 9, v[20:21]
	v_cvt_pk_bf16_f32 v23, v35, s0
	v_lshl_add_u64 v[20:21], v[48:49], 0, v[20:21]
	global_store_short v[20:21], v23, off
	v_add_u32_e32 v20, 48, v22
	v_add_u32_e32 v21, 3, v24
	v_cndmask_b32_e64 v20, v21, v20, s[38:39]
	v_ashrrev_i32_e32 v21, 31, v20
	v_lshl_add_u64 v[20:21], s[6:7], 0, v[20:21]
	v_lshlrev_b64 v[20:21], 9, v[20:21]
	v_lshl_add_u64 v[20:21], v[48:49], 0, v[20:21]
	global_store_short v[20:21], v16, off
	v_cvt_pk_bf16_f32 v20, v17, s0
	v_add_u32_e32 v16, 49, v22
	v_add_u32_e32 v17, 2, v24
	v_cndmask_b32_e64 v16, v17, v16, s[38:39]
	v_ashrrev_i32_e32 v17, 31, v16
	v_lshl_add_u64 v[16:17], s[6:7], 0, v[16:17]
	v_lshlrev_b64 v[16:17], 9, v[16:17]
	v_lshl_add_u64 v[16:17], v[48:49], 0, v[16:17]
	global_store_short v[16:17], v20, off
	v_add_u32_e32 v16, 50, v22
	v_add_u32_e32 v17, 1, v24
	v_cndmask_b32_e64 v16, v17, v16, s[38:39]
	v_ashrrev_i32_e32 v17, 31, v16
	v_lshl_add_u64 v[16:17], s[6:7], 0, v[16:17]
	v_lshlrev_b64 v[16:17], 9, v[16:17]
	v_lshl_add_u64 v[16:17], v[48:49], 0, v[16:17]
	global_store_short v[16:17], v18, off
	v_add_u32_e32 v16, 51, v22
	v_cndmask_b32_e64 v16, v24, v16, s[38:39]
	v_ashrrev_i32_e32 v17, 31, v16
	v_lshl_add_u64 v[16:17], s[6:7], 0, v[16:17]
	v_lshlrev_b64 v[16:17], 9, v[16:17]
	s_add_i32 s48, s48, 64
	v_cvt_pk_bf16_f32 v18, v19, s0
	v_lshl_add_u64 v[16:17], v[48:49], 0, v[16:17]
	v_subrev_u32_e32 v64, 64, v64
	s_cmpk_eq_i32 s48, 0x1100
	s_mov_b32 s28, s43
	global_store_short v[16:17], v18, off
	s_cbranch_scc1 .LBB0_612

.LBB0_665:
	s_ashr_i32 s71, s70, 31
	s_lshl_b64 s[28:29], s[70:71], 18
	s_add_u32 s78, s3, s28
	s_addc_u32 s79, s9, s29
	s_and_b64 s[28:29], s[76:77], exec
	s_cselect_b32 s37, s79, s83
	s_cselect_b32 s50, s78, s82
	s_ashr_i32 s73, s72, 31
	s_lshl_b64 s[28:29], s[72:73], 18
	s_add_u32 s28, s69, s28
	s_addc_u32 s29, s60, s29
	s_add_u32 s80, s28, 0xffd00000
	s_addc_u32 s81, s29, -1
	s_and_b64 s[28:29], s[76:77], exec
	s_cselect_b32 s51, s81, s97
	s_cselect_b32 s71, s80, s96
	s_add_u32 s82, s82, 0x20080
	s_addc_u32 s83, s83, 0
	s_add_u32 s73, s96, 0x100
	s_addc_u32 s75, s97, 0
	s_mov_b32 s84, -2
.Lpeel_gate:
	s_add_u32 s28, s82, 0xfffe0080
	s_addc_u32 s29, s83, -1
	s_add_i32 s85, 0, 0x10000
	s_cmp_eq_u32 s84, 4
	s_cselect_b32 vcc_hi, s37, s29
	s_cselect_b32 vcc_lo, s50, s28
	s_cselect_b32 s97, s51, s75
	s_cselect_b32 s96, s71, s73
	s_add_i32 s28, 0, 0x14000
	v_add_u32_e32 v0, s85, v183
	v_add_u32_e32 v12, s28, v183
	ds_read_b128 v[16:19], v0
	ds_read_b128 v[20:23], v0 offset:1024
	ds_read_b128 v[24:27], v0 offset:2048
	ds_read_b128 v[28:31], v0 offset:3072
	ds_read_b128 v[0:3], v12
	ds_read_b128 v[4:7], v12 offset:1024
	ds_read_b128 v[8:11], v12 offset:2048
	ds_read_b128 v[12:15], v12 offset:3072
	v_lshl_add_u64 v[194:195], s[82:83], 0, v[170:171]
	s_add_i32 m0, s6, 0xc000
	ds_read_b128 v[174:177], v184
	ds_read_b128 v[178:181], v184 offset:1024
	ds_read_b128 v[186:189], v184 offset:2048
	ds_read_b128 v[190:193], v184 offset:3072
	ds_read_b128 v[216:219], v184 offset:4096
	ds_read_b128 v[220:223], v184 offset:5120
	ds_read_b128 v[224:227], v184 offset:6144
	ds_read_b128 v[228:231], v184 offset:7168
	global_load_lds_dwordx4 v[194:195], off
	v_lshl_add_u64 v[194:195], s[82:83], 0, v[172:173]
	s_add_i32 m0, s6, 0xe000
	s_nop 0
	global_load_lds_dwordx4 v[194:195], off
	s_waitcnt vmcnt(8)
	s_waitcnt lgkmcnt(0)
	s_barrier
	s_setprio 1
	s_waitcnt lgkmcnt(0)
	v_mfma_scale_f32_16x16x128_f8f6f4 v[158:161], v[16:23], v[174:181], 0, v200, v201 op_sel_hi:[0,0,0]
	v_mfma_scale_f32_16x16x128_f8f6f4 v[154:157], v[24:31], v[174:181], 0, v200, v201 op_sel_hi:[0,0,0]
	v_mfma_scale_f32_16x16x128_f8f6f4 v[150:153], v[16:23], v[186:193], 0, v200, v201 op_sel_hi:[0,0,0]
	v_mfma_scale_f32_16x16x128_f8f6f4 v[146:149], v[24:31], v[186:193], 0, v200, v201 op_sel_hi:[0,0,0]
	v_mfma_scale_f32_16x16x128_f8f6f4 v[134:137], v[16:23], v[216:223], 0, v200, v201 op_sel_hi:[0,0,0]
	v_mfma_scale_f32_16x16x128_f8f6f4 v[130:133], v[24:31], v[216:223], 0, v200, v201 op_sel_hi:[0,0,0]
	v_mfma_scale_f32_16x16x128_f8f6f4 v[118:121], v[16:23], v[224:231], 0, v200, v201 op_sel_hi:[0,0,0]
	v_mfma_scale_f32_16x16x128_f8f6f4 v[114:117], v[24:31], v[224:231], 0, v200, v201 op_sel_hi:[0,0,0]
	s_setprio 0
	s_setprio 1
	v_mfma_scale_f32_16x16x128_f8f6f4 v[142:145], v[0:7], v[174:181], 0, v200, v201 op_sel_hi:[0,0,0]
	v_mfma_scale_f32_16x16x128_f8f6f4 v[138:141], v[8:15], v[174:181], 0, v200, v201 op_sel_hi:[0,0,0]
	v_mfma_scale_f32_16x16x128_f8f6f4 v[126:129], v[0:7], v[186:193], 0, v200, v201 op_sel_hi:[0,0,0]
	v_mfma_scale_f32_16x16x128_f8f6f4 v[122:125], v[8:15], v[186:193], 0, v200, v201 op_sel_hi:[0,0,0]
	v_mfma_scale_f32_16x16x128_f8f6f4 v[108:111], v[0:7], v[216:223], 0, v200, v201 op_sel_hi:[0,0,0]
	v_mfma_scale_f32_16x16x128_f8f6f4 v[104:107], v[8:15], v[216:223], 0, v200, v201 op_sel_hi:[0,0,0]
	v_mfma_scale_f32_16x16x128_f8f6f4 v[100:103], v[0:7], v[224:231], 0, v200, v201 op_sel_hi:[0,0,0]
	v_mfma_scale_f32_16x16x128_f8f6f4 v[96:99], v[8:15], v[224:231], 0, v200, v201 op_sel_hi:[0,0,0]
	s_setprio 0
	s_barrier
	s_add_i32 s29, s85, s14
	v_lshl_add_u64 v[174:175], s[96:97], 0, v[164:165]
	s_mov_b32 m0, s29
	ds_read_b128 v[186:189], v184 offset:16384
	ds_read_b128 v[190:193], v184 offset:17408
	ds_read_b128 v[216:219], v184 offset:18432
	ds_read_b128 v[220:223], v184 offset:19456
	ds_read_b128 v[224:227], v184 offset:20480
	ds_read_b128 v[228:231], v184 offset:21504
	ds_read_b128 v[232:235], v184 offset:22528
	ds_read_b128 v[236:239], v184 offset:23552
	global_load_lds_dwordx4 v[174:175], off
	s_add_i32 m0, s29, 0x2000
	s_add_u32 s30, s96, 0x20000
	v_lshl_add_u64 v[176:177], s[96:97], 0, v[168:169]
	s_addc_u32 s31, s97, 0
	s_add_i32 s28, s28, s14
	global_load_lds_dwordx4 v[176:177], off
	v_lshl_add_u64 v[178:179], s[30:31], 0, v[164:165]
	s_mov_b32 m0, s28
	v_lshl_add_u64 v[180:181], vcc, 0, v[166:167]
	global_load_lds_dwordx4 v[178:179], off
	v_lshl_add_u64 v[178:179], s[30:31], 0, v[168:169]
	s_add_i32 m0, s28, 0x2000
	s_nop 0
	global_load_lds_dwordx4 v[178:179], off
	v_lshl_add_u64 v[178:179], vcc, 0, v[162:163]
	s_mov_b32 m0, s6
	s_nop 0
	global_load_lds_dwordx4 v[178:179], off
	s_mov_b32 m0, s7
	s_nop 0
	global_load_lds_dwordx4 v[180:181], off
	s_waitcnt vmcnt(8)
	s_waitcnt lgkmcnt(0)
	s_barrier
	s_setprio 1
	s_waitcnt lgkmcnt(0)
	v_mfma_scale_f32_16x16x128_f8f6f4 v[92:95], v[16:23], v[186:193], 0, v200, v201 op_sel_hi:[0,0,0]
	v_mfma_scale_f32_16x16x128_f8f6f4 v[88:91], v[24:31], v[186:193], 0, v200, v201 op_sel_hi:[0,0,0]
	v_mfma_scale_f32_16x16x128_f8f6f4 v[84:87], v[16:23], v[216:223], 0, v200, v201 op_sel_hi:[0,0,0]
	v_mfma_scale_f32_16x16x128_f8f6f4 v[80:83], v[24:31], v[216:223], 0, v200, v201 op_sel_hi:[0,0,0]
	v_mfma_scale_f32_16x16x128_f8f6f4 v[68:71], v[16:23], v[224:231], 0, v200, v201 op_sel_hi:[0,0,0]
	v_mfma_scale_f32_16x16x128_f8f6f4 v[64:67], v[24:31], v[224:231], 0, v200, v201 op_sel_hi:[0,0,0]
	v_mfma_scale_f32_16x16x128_f8f6f4 v[52:55], v[16:23], v[232:239], 0, v200, v201 op_sel_hi:[0,0,0]
	v_mfma_scale_f32_16x16x128_f8f6f4 v[48:51], v[24:31], v[232:239], 0, v200, v201 op_sel_hi:[0,0,0]
	s_setprio 0
	s_setprio 1
	v_mfma_scale_f32_16x16x128_f8f6f4 v[76:79], v[0:7], v[186:193], 0, v200, v201 op_sel_hi:[0,0,0]
	v_mfma_scale_f32_16x16x128_f8f6f4 v[72:75], v[8:15], v[186:193], 0, v200, v201 op_sel_hi:[0,0,0]
	v_mfma_scale_f32_16x16x128_f8f6f4 v[60:63], v[0:7], v[216:223], 0, v200, v201 op_sel_hi:[0,0,0]
	v_mfma_scale_f32_16x16x128_f8f6f4 v[56:59], v[8:15], v[216:223], 0, v200, v201 op_sel_hi:[0,0,0]
	v_mfma_scale_f32_16x16x128_f8f6f4 v[44:47], v[0:7], v[224:231], 0, v200, v201 op_sel_hi:[0,0,0]
	v_mfma_scale_f32_16x16x128_f8f6f4 v[40:43], v[8:15], v[224:231], 0, v200, v201 op_sel_hi:[0,0,0]
	v_mfma_scale_f32_16x16x128_f8f6f4 v[36:39], v[0:7], v[232:239], 0, v200, v201 op_sel_hi:[0,0,0]
	v_mfma_scale_f32_16x16x128_f8f6f4 v[32:35], v[8:15], v[232:239], 0, v200, v201 op_sel_hi:[0,0,0]
	s_setprio 0
	s_barrier
	s_add_i32 s30, 0, 0x18000
	s_add_i32 s31, 0, 0x1c000
	v_add_u32_e32 v12, s30, v183
	v_add_u32_e32 v28, s31, v183
	ds_read_b128 v[0:3], v12
	ds_read_b128 v[4:7], v12 offset:1024
	ds_read_b128 v[8:11], v12 offset:2048
	ds_read_b128 v[12:15], v12 offset:3072
	ds_read_b128 v[16:19], v28
	ds_read_b128 v[20:23], v28 offset:1024
	ds_read_b128 v[24:27], v28 offset:2048
	ds_read_b128 v[28:31], v28 offset:3072
	s_add_u32 s28, vcc_lo, 0x20000
	s_addc_u32 s29, vcc_hi, 0
	s_mov_b32 m0, s86
	v_lshl_add_u64 v[194:195], s[28:29], 0, v[162:163]
	ds_read_b128 v[186:189], v184 offset:32768
	ds_read_b128 v[190:193], v184 offset:33792
	ds_read_b128 v[216:219], v184 offset:34816
	ds_read_b128 v[220:223], v184 offset:35840
	ds_read_b128 v[224:227], v184 offset:36864
	ds_read_b128 v[228:231], v184 offset:37888
	ds_read_b128 v[232:235], v184 offset:38912
	ds_read_b128 v[236:239], v184 offset:39936
	global_load_lds_dwordx4 v[194:195], off
	v_lshl_add_u64 v[194:195], s[28:29], 0, v[166:167]
	s_mov_b32 m0, s33
	s_nop 0
	global_load_lds_dwordx4 v[194:195], off
	s_waitcnt vmcnt(8)
	s_waitcnt lgkmcnt(0)
	s_barrier
	s_setprio 1
	s_waitcnt lgkmcnt(0)
	v_mfma_scale_f32_16x16x128_f8f6f4 v[158:161], v[0:7], v[186:193], v[158:161], v200, v201 op_sel_hi:[0,0,0]
	v_mfma_scale_f32_16x16x128_f8f6f4 v[154:157], v[8:15], v[186:193], v[154:157], v200, v201 op_sel_hi:[0,0,0]
	v_mfma_scale_f32_16x16x128_f8f6f4 v[150:153], v[0:7], v[216:223], v[150:153], v200, v201 op_sel_hi:[0,0,0]
	v_mfma_scale_f32_16x16x128_f8f6f4 v[146:149], v[8:15], v[216:223], v[146:149], v200, v201 op_sel_hi:[0,0,0]
	v_mfma_scale_f32_16x16x128_f8f6f4 v[134:137], v[0:7], v[224:231], v[134:137], v200, v201 op_sel_hi:[0,0,0]
	v_mfma_scale_f32_16x16x128_f8f6f4 v[130:133], v[8:15], v[224:231], v[130:133], v200, v201 op_sel_hi:[0,0,0]
	v_mfma_scale_f32_16x16x128_f8f6f4 v[118:121], v[0:7], v[232:239], v[118:121], v200, v201 op_sel_hi:[0,0,0]
	v_mfma_scale_f32_16x16x128_f8f6f4 v[114:117], v[8:15], v[232:239], v[114:117], v200, v201 op_sel_hi:[0,0,0]
	s_setprio 0
	s_setprio 1
	v_mfma_scale_f32_16x16x128_f8f6f4 v[142:145], v[16:23], v[186:193], v[142:145], v200, v201 op_sel_hi:[0,0,0]
	v_mfma_scale_f32_16x16x128_f8f6f4 v[138:141], v[24:31], v[186:193], v[138:141], v200, v201 op_sel_hi:[0,0,0]
	v_mfma_scale_f32_16x16x128_f8f6f4 v[126:129], v[16:23], v[216:223], v[126:129], v200, v201 op_sel_hi:[0,0,0]
	v_mfma_scale_f32_16x16x128_f8f6f4 v[122:125], v[24:31], v[216:223], v[122:125], v200, v201 op_sel_hi:[0,0,0]
	v_mfma_scale_f32_16x16x128_f8f6f4 v[108:111], v[16:23], v[224:231], v[108:111], v200, v201 op_sel_hi:[0,0,0]
	v_mfma_scale_f32_16x16x128_f8f6f4 v[104:107], v[24:31], v[224:231], v[104:107], v200, v201 op_sel_hi:[0,0,0]
	v_mfma_scale_f32_16x16x128_f8f6f4 v[100:103], v[16:23], v[232:239], v[100:103], v200, v201 op_sel_hi:[0,0,0]
	v_mfma_scale_f32_16x16x128_f8f6f4 v[96:99], v[24:31], v[232:239], v[96:99], v200, v201 op_sel_hi:[0,0,0]
	s_setprio 0
	s_barrier
	s_add_i32 s28, s30, s14
	v_lshl_add_u64 v[174:175], v[174:175], 0, s[56:57]
	s_mov_b32 m0, s28
	ds_read_b128 v[186:189], v184 offset:49152
	ds_read_b128 v[190:193], v184 offset:50176
	ds_read_b128 v[216:219], v184 offset:51200
	ds_read_b128 v[220:223], v184 offset:52224
	ds_read_b128 v[224:227], v184 offset:53248
	ds_read_b128 v[228:231], v184 offset:54272
	ds_read_b128 v[232:235], v184 offset:55296
	ds_read_b128 v[236:239], v184 offset:56320
	global_load_lds_dwordx4 v[174:175], off
	s_add_i32 m0, s28, 0x2000
	s_add_u32 s28, s96, 0x20080
	v_lshl_add_u64 v[174:175], v[176:177], 0, s[56:57]
	s_addc_u32 s29, s97, 0
	s_add_i32 s30, s31, s14
	global_load_lds_dwordx4 v[174:175], off
	v_lshl_add_u64 v[174:175], s[28:29], 0, v[164:165]
	s_mov_b32 m0, s30
	s_nop 0
	global_load_lds_dwordx4 v[174:175], off
	v_lshl_add_u64 v[174:175], s[28:29], 0, v[168:169]
	s_add_i32 m0, s30, 0x2000
	s_nop 0
	global_load_lds_dwordx4 v[174:175], off
	v_lshl_add_u64 v[174:175], v[178:179], 0, s[56:57]
	s_mov_b32 m0, s54
	s_nop 0
	global_load_lds_dwordx4 v[174:175], off
	v_lshl_add_u64 v[174:175], v[180:181], 0, s[56:57]
	s_mov_b32 m0, s55
	s_nop 0
	global_load_lds_dwordx4 v[174:175], off
	s_waitcnt vmcnt(8)
	s_waitcnt lgkmcnt(0)
	s_barrier
	s_setprio 1
	s_waitcnt lgkmcnt(0)
	v_mfma_scale_f32_16x16x128_f8f6f4 v[92:95], v[0:7], v[186:193], v[92:95], v200, v201 op_sel_hi:[0,0,0]
	v_mfma_scale_f32_16x16x128_f8f6f4 v[88:91], v[8:15], v[186:193], v[88:91], v200, v201 op_sel_hi:[0,0,0]
	v_mfma_scale_f32_16x16x128_f8f6f4 v[84:87], v[0:7], v[216:223], v[84:87], v200, v201 op_sel_hi:[0,0,0]
	v_mfma_scale_f32_16x16x128_f8f6f4 v[80:83], v[8:15], v[216:223], v[80:83], v200, v201 op_sel_hi:[0,0,0]
	v_mfma_scale_f32_16x16x128_f8f6f4 v[68:71], v[0:7], v[224:231], v[68:71], v200, v201 op_sel_hi:[0,0,0]
	v_mfma_scale_f32_16x16x128_f8f6f4 v[64:67], v[8:15], v[224:231], v[64:67], v200, v201 op_sel_hi:[0,0,0]
	v_mfma_scale_f32_16x16x128_f8f6f4 v[52:55], v[0:7], v[232:239], v[52:55], v200, v201 op_sel_hi:[0,0,0]
	v_mfma_scale_f32_16x16x128_f8f6f4 v[48:51], v[8:15], v[232:239], v[48:51], v200, v201 op_sel_hi:[0,0,0]
	s_setprio 0
	s_setprio 1
	v_mfma_scale_f32_16x16x128_f8f6f4 v[76:79], v[16:23], v[186:193], v[76:79], v200, v201 op_sel_hi:[0,0,0]
	v_mfma_scale_f32_16x16x128_f8f6f4 v[72:75], v[24:31], v[186:193], v[72:75], v200, v201 op_sel_hi:[0,0,0]
	v_mfma_scale_f32_16x16x128_f8f6f4 v[60:63], v[16:23], v[216:223], v[60:63], v200, v201 op_sel_hi:[0,0,0]
	v_mfma_scale_f32_16x16x128_f8f6f4 v[56:59], v[24:31], v[216:223], v[56:59], v200, v201 op_sel_hi:[0,0,0]
	v_mfma_scale_f32_16x16x128_f8f6f4 v[44:47], v[16:23], v[224:231], v[44:47], v200, v201 op_sel_hi:[0,0,0]
	v_mfma_scale_f32_16x16x128_f8f6f4 v[40:43], v[24:31], v[224:231], v[40:43], v200, v201 op_sel_hi:[0,0,0]
	v_mfma_scale_f32_16x16x128_f8f6f4 v[36:39], v[16:23], v[232:239], v[36:39], v200, v201 op_sel_hi:[0,0,0]
	v_mfma_scale_f32_16x16x128_f8f6f4 v[32:35], v[24:31], v[232:239], v[32:35], v200, v201 op_sel_hi:[0,0,0]
	s_setprio 0
	s_barrier
	s_add_i32 s84, s84, 2
	s_add_u32 s82, s82, 0x100
	s_addc_u32 s83, s83, 0
	s_add_u32 s73, s73, 0x100
	s_addc_u32 s75, s75, 0
	s_cmp_gt_u32 s84, 5

.LBB0_835:
	s_ashr_i32 s71, s70, 31
	s_lshl_b64 s[28:29], s[70:71], 19
	s_add_u32 s72, s10, s28
	s_addc_u32 s73, s11, s29
	s_and_b64 s[28:29], s[40:41], exec
	s_cselect_b32 s37, s73, s79
	s_cselect_b32 s50, s72, s78
	s_ashr_i32 s65, s64, 31
	s_lshl_b64 s[28:29], s[64:65], 19
	s_add_u32 s74, s15, s28
	s_addc_u32 s75, s25, s29
	s_and_b64 s[28:29], s[40:41], exec
	s_cselect_b32 s51, s75, s81
	s_cselect_b32 s65, s74, s80
	s_add_u32 s78, s78, 0x40080
	s_addc_u32 s79, s79, 0
	s_add_u32 s71, s80, 0x100
	s_addc_u32 s77, s81, 0
	s_mov_b32 s84, -2
.Lpeel_wo:
	s_add_u32 s28, s78, 0xfffc0080
	s_addc_u32 s29, s79, -1
	s_add_i32 s30, 0, 0x10000
	s_cmp_eq_u32 s84, 12
	s_cselect_b32 s83, s37, s29
	s_cselect_b32 s82, s50, s28
	v_add_u32_e32 v112, s30, v183
	s_cselect_b32 s81, s51, s77
	s_cselect_b32 s80, s65, s71
	s_add_i32 s31, 0, 0x14000
	ds_read_b128 v[130:133], v112
	ds_read_b128 v[134:137], v112 offset:1024
	ds_read_b128 v[150:153], v112 offset:2048
	ds_read_b128 v[154:157], v112 offset:3072
	v_add_u32_e32 v112, s31, v183
	ds_read_b128 v[158:161], v112
	ds_read_b128 v[162:165], v112 offset:1024
	ds_read_b128 v[166:169], v112 offset:2048
	ds_read_b128 v[170:173], v112 offset:3072
	v_lshl_add_u64 v[194:195], s[78:79], 0, v[146:147]
	s_add_i32 m0, s34, 0xc000
	ds_read_b128 v[174:177], v184
	ds_read_b128 v[178:181], v184 offset:1024
	ds_read_b128 v[186:189], v184 offset:2048
	ds_read_b128 v[190:193], v184 offset:3072
	ds_read_b128 v[206:209], v184 offset:4096
	ds_read_b128 v[210:213], v184 offset:5120
	ds_read_b128 v[216:219], v184 offset:6144
	ds_read_b128 v[220:223], v184 offset:7168
	global_load_lds_dwordx4 v[194:195], off
	v_lshl_add_u64 v[194:195], s[78:79], 0, v[148:149]
	s_add_i32 m0, s34, 0xe000
	s_nop 0
	global_load_lds_dwordx4 v[194:195], off
	s_waitcnt vmcnt(8)
	s_waitcnt lgkmcnt(0)
	s_barrier
	s_setprio 1
	s_waitcnt lgkmcnt(0)
	v_mfma_f32_16x16x32_bf16 v[126:129], v[130:133], v[174:177], 0
	v_mfma_f32_16x16x32_bf16 v[122:125], v[150:153], v[174:177], 0
	v_mfma_f32_16x16x32_bf16 v[118:121], v[130:133], v[186:189], 0
	v_mfma_f32_16x16x32_bf16 v[114:117], v[150:153], v[186:189], 0
	v_mfma_f32_16x16x32_bf16 v[108:111], v[130:133], v[206:209], 0
	v_mfma_f32_16x16x32_bf16 v[104:107], v[150:153], v[206:209], 0
	v_mfma_f32_16x16x32_bf16 v[100:103], v[130:133], v[216:219], 0
	v_mfma_f32_16x16x32_bf16 v[96:99], v[150:153], v[216:219], 0
	v_mfma_f32_16x16x32_bf16 v[126:129], v[134:137], v[178:181], v[126:129]
	v_mfma_f32_16x16x32_bf16 v[122:125], v[154:157], v[178:181], v[122:125]
	v_mfma_f32_16x16x32_bf16 v[118:121], v[134:137], v[190:193], v[118:121]
	v_mfma_f32_16x16x32_bf16 v[114:117], v[154:157], v[190:193], v[114:117]
	v_mfma_f32_16x16x32_bf16 v[108:111], v[134:137], v[210:213], v[108:111]
	v_mfma_f32_16x16x32_bf16 v[104:107], v[154:157], v[210:213], v[104:107]
	v_mfma_f32_16x16x32_bf16 v[100:103], v[134:137], v[220:223], v[100:103]
	v_mfma_f32_16x16x32_bf16 v[96:99], v[154:157], v[220:223], v[96:99]
	s_setprio 0
	s_setprio 1
	v_mfma_f32_16x16x32_bf16 v[60:63], v[158:161], v[174:177], 0
	v_mfma_f32_16x16x32_bf16 v[56:59], v[166:169], v[174:177], 0
	v_mfma_f32_16x16x32_bf16 v[52:55], v[158:161], v[186:189], 0
	v_mfma_f32_16x16x32_bf16 v[48:51], v[166:169], v[186:189], 0
	v_mfma_f32_16x16x32_bf16 v[44:47], v[158:161], v[206:209], 0
	v_mfma_f32_16x16x32_bf16 v[40:43], v[166:169], v[206:209], 0
	v_mfma_f32_16x16x32_bf16 v[36:39], v[158:161], v[216:219], 0
	v_mfma_f32_16x16x32_bf16 v[32:35], v[166:169], v[216:219], 0
	v_mfma_f32_16x16x32_bf16 v[60:63], v[162:165], v[178:181], v[60:63]
	v_mfma_f32_16x16x32_bf16 v[56:59], v[170:173], v[178:181], v[56:59]
	v_mfma_f32_16x16x32_bf16 v[52:55], v[162:165], v[190:193], v[52:55]
	v_mfma_f32_16x16x32_bf16 v[48:51], v[170:173], v[190:193], v[48:51]
	v_mfma_f32_16x16x32_bf16 v[44:47], v[162:165], v[210:213], v[44:47]
	v_mfma_f32_16x16x32_bf16 v[40:43], v[170:173], v[210:213], v[40:43]
	v_mfma_f32_16x16x32_bf16 v[36:39], v[162:165], v[220:223], v[36:39]
	v_mfma_f32_16x16x32_bf16 v[32:35], v[170:173], v[220:223], v[32:35]
	s_setprio 0
	s_barrier
	s_add_i32 s28, s30, s33
	v_lshl_add_u64 v[194:195], s[80:81], 0, v[140:141]
	s_mov_b32 m0, s28
	ds_read_b128 v[174:177], v184 offset:16384
	ds_read_b128 v[178:181], v184 offset:17408
	ds_read_b128 v[186:189], v184 offset:18432
	ds_read_b128 v[190:193], v184 offset:19456
	ds_read_b128 v[206:209], v184 offset:20480
	ds_read_b128 v[210:213], v184 offset:21504
	ds_read_b128 v[216:219], v184 offset:22528
	ds_read_b128 v[220:223], v184 offset:23552
	global_load_lds_dwordx4 v[194:195], off
	s_add_i32 m0, s28, 0x2000
	s_add_u32 s28, s80, 0x40000
	v_lshl_add_u64 v[224:225], s[80:81], 0, v[144:145]
	s_addc_u32 s29, s81, 0
	s_add_i32 s30, s31, s33
	global_load_lds_dwordx4 v[224:225], off
	v_lshl_add_u64 v[226:227], s[28:29], 0, v[140:141]
	s_mov_b32 m0, s30
	v_lshl_add_u64 v[228:229], s[82:83], 0, v[142:143]
	global_load_lds_dwordx4 v[226:227], off
	v_lshl_add_u64 v[226:227], s[28:29], 0, v[144:145]
	s_add_i32 m0, s30, 0x2000
	s_nop 0
	global_load_lds_dwordx4 v[226:227], off
	v_lshl_add_u64 v[226:227], s[82:83], 0, v[138:139]
	s_mov_b32 m0, s34
	s_nop 0
	global_load_lds_dwordx4 v[226:227], off
	s_mov_b32 m0, s54
	s_nop 0
	global_load_lds_dwordx4 v[228:229], off
	s_waitcnt vmcnt(8)
	s_waitcnt lgkmcnt(0)
	s_barrier
	s_setprio 1
	s_waitcnt lgkmcnt(0)
	v_mfma_f32_16x16x32_bf16 v[92:95], v[130:133], v[174:177], 0
	v_mfma_f32_16x16x32_bf16 v[88:91], v[150:153], v[174:177], 0
	v_mfma_f32_16x16x32_bf16 v[84:87], v[130:133], v[186:189], 0
	v_mfma_f32_16x16x32_bf16 v[80:83], v[150:153], v[186:189], 0
	v_mfma_f32_16x16x32_bf16 v[76:79], v[130:133], v[206:209], 0
	v_mfma_f32_16x16x32_bf16 v[72:75], v[150:153], v[206:209], 0
	v_mfma_f32_16x16x32_bf16 v[68:71], v[130:133], v[216:219], 0
	v_mfma_f32_16x16x32_bf16 v[64:67], v[150:153], v[216:219], 0
	v_mfma_f32_16x16x32_bf16 v[92:95], v[134:137], v[178:181], v[92:95]
	v_mfma_f32_16x16x32_bf16 v[88:91], v[154:157], v[178:181], v[88:91]
	v_mfma_f32_16x16x32_bf16 v[84:87], v[134:137], v[190:193], v[84:87]
	v_mfma_f32_16x16x32_bf16 v[80:83], v[154:157], v[190:193], v[80:83]
	v_mfma_f32_16x16x32_bf16 v[76:79], v[134:137], v[210:213], v[76:79]
	v_mfma_f32_16x16x32_bf16 v[72:75], v[154:157], v[210:213], v[72:75]
	v_mfma_f32_16x16x32_bf16 v[68:71], v[134:137], v[220:223], v[68:71]
	v_mfma_f32_16x16x32_bf16 v[64:67], v[154:157], v[220:223], v[64:67]
	s_setprio 0
	s_setprio 1
	v_mfma_f32_16x16x32_bf16 v[28:31], v[158:161], v[174:177], 0
	v_mfma_f32_16x16x32_bf16 v[24:27], v[166:169], v[174:177], 0
	v_mfma_f32_16x16x32_bf16 v[20:23], v[158:161], v[186:189], 0
	v_mfma_f32_16x16x32_bf16 v[16:19], v[166:169], v[186:189], 0
	v_mfma_f32_16x16x32_bf16 v[12:15], v[158:161], v[206:209], 0
	v_mfma_f32_16x16x32_bf16 v[8:11], v[166:169], v[206:209], 0
	v_mfma_f32_16x16x32_bf16 v[4:7], v[158:161], v[216:219], 0
	v_mfma_f32_16x16x32_bf16 v[0:3], v[166:169], v[216:219], 0
	v_mfma_f32_16x16x32_bf16 v[28:31], v[162:165], v[178:181], v[28:31]
	v_mfma_f32_16x16x32_bf16 v[24:27], v[170:173], v[178:181], v[24:27]
	v_mfma_f32_16x16x32_bf16 v[20:23], v[162:165], v[190:193], v[20:23]
	v_mfma_f32_16x16x32_bf16 v[16:19], v[170:173], v[190:193], v[16:19]
	v_mfma_f32_16x16x32_bf16 v[12:15], v[162:165], v[210:213], v[12:15]
	v_mfma_f32_16x16x32_bf16 v[8:11], v[170:173], v[210:213], v[8:11]
	v_mfma_f32_16x16x32_bf16 v[4:7], v[162:165], v[220:223], v[4:7]
	v_mfma_f32_16x16x32_bf16 v[0:3], v[170:173], v[220:223], v[0:3]
	s_setprio 0
	s_barrier
	s_add_i32 s30, 0, 0x18000
	v_add_u32_e32 v112, s30, v183
	s_add_i32 s31, 0, 0x1c000
	ds_read_b128 v[130:133], v112
	ds_read_b128 v[134:137], v112 offset:1024
	ds_read_b128 v[150:153], v112 offset:2048
	ds_read_b128 v[154:157], v112 offset:3072
	v_add_u32_e32 v112, s31, v183
	ds_read_b128 v[158:161], v112
	ds_read_b128 v[162:165], v112 offset:1024
	ds_read_b128 v[166:169], v112 offset:2048
	ds_read_b128 v[170:173], v112 offset:3072
	s_add_u32 s28, s82, 0x40000
	s_addc_u32 s29, s83, 0
	s_mov_b32 m0, s55
	v_lshl_add_u64 v[230:231], s[28:29], 0, v[138:139]
	ds_read_b128 v[174:177], v184 offset:32768
	ds_read_b128 v[178:181], v184 offset:33792
	ds_read_b128 v[186:189], v184 offset:34816
	ds_read_b128 v[190:193], v184 offset:35840
	ds_read_b128 v[206:209], v184 offset:36864
	ds_read_b128 v[210:213], v184 offset:37888
	ds_read_b128 v[216:219], v184 offset:38912
	ds_read_b128 v[220:223], v184 offset:39936
	global_load_lds_dwordx4 v[230:231], off
	v_lshl_add_u64 v[230:231], s[28:29], 0, v[142:143]
	s_mov_b32 m0, s58
	s_nop 0
	global_load_lds_dwordx4 v[230:231], off
	s_waitcnt vmcnt(8)
	s_waitcnt lgkmcnt(0)
	s_barrier
	s_setprio 1
	s_waitcnt lgkmcnt(0)
	v_mfma_f32_16x16x32_bf16 v[126:129], v[130:133], v[174:177], v[126:129]
	v_mfma_f32_16x16x32_bf16 v[122:125], v[150:153], v[174:177], v[122:125]
	v_mfma_f32_16x16x32_bf16 v[118:121], v[130:133], v[186:189], v[118:121]
	v_mfma_f32_16x16x32_bf16 v[114:117], v[150:153], v[186:189], v[114:117]
	v_mfma_f32_16x16x32_bf16 v[108:111], v[130:133], v[206:209], v[108:111]
	v_mfma_f32_16x16x32_bf16 v[104:107], v[150:153], v[206:209], v[104:107]
	v_mfma_f32_16x16x32_bf16 v[100:103], v[130:133], v[216:219], v[100:103]
	v_mfma_f32_16x16x32_bf16 v[96:99], v[150:153], v[216:219], v[96:99]
	v_mfma_f32_16x16x32_bf16 v[126:129], v[134:137], v[178:181], v[126:129]
	v_mfma_f32_16x16x32_bf16 v[122:125], v[154:157], v[178:181], v[122:125]
	v_mfma_f32_16x16x32_bf16 v[118:121], v[134:137], v[190:193], v[118:121]
	v_mfma_f32_16x16x32_bf16 v[114:117], v[154:157], v[190:193], v[114:117]
	v_mfma_f32_16x16x32_bf16 v[108:111], v[134:137], v[210:213], v[108:111]
	v_mfma_f32_16x16x32_bf16 v[104:107], v[154:157], v[210:213], v[104:107]
	v_mfma_f32_16x16x32_bf16 v[100:103], v[134:137], v[220:223], v[100:103]
	v_mfma_f32_16x16x32_bf16 v[96:99], v[154:157], v[220:223], v[96:99]
	s_setprio 0
	s_setprio 1
	v_mfma_f32_16x16x32_bf16 v[60:63], v[158:161], v[174:177], v[60:63]
	v_mfma_f32_16x16x32_bf16 v[56:59], v[166:169], v[174:177], v[56:59]
	v_mfma_f32_16x16x32_bf16 v[52:55], v[158:161], v[186:189], v[52:55]
	v_mfma_f32_16x16x32_bf16 v[48:51], v[166:169], v[186:189], v[48:51]
	v_mfma_f32_16x16x32_bf16 v[44:47], v[158:161], v[206:209], v[44:47]
	v_mfma_f32_16x16x32_bf16 v[40:43], v[166:169], v[206:209], v[40:43]
	v_mfma_f32_16x16x32_bf16 v[36:39], v[158:161], v[216:219], v[36:39]
	v_mfma_f32_16x16x32_bf16 v[32:35], v[166:169], v[216:219], v[32:35]
	v_mfma_f32_16x16x32_bf16 v[60:63], v[162:165], v[178:181], v[60:63]
	v_mfma_f32_16x16x32_bf16 v[56:59], v[170:173], v[178:181], v[56:59]
	v_mfma_f32_16x16x32_bf16 v[52:55], v[162:165], v[190:193], v[52:55]
	v_mfma_f32_16x16x32_bf16 v[48:51], v[170:173], v[190:193], v[48:51]
	v_mfma_f32_16x16x32_bf16 v[44:47], v[162:165], v[210:213], v[44:47]
	v_mfma_f32_16x16x32_bf16 v[40:43], v[170:173], v[210:213], v[40:43]
	v_mfma_f32_16x16x32_bf16 v[36:39], v[162:165], v[220:223], v[36:39]
	v_mfma_f32_16x16x32_bf16 v[32:35], v[170:173], v[220:223], v[32:35]
	s_setprio 0
	s_barrier
	s_add_i32 s28, s30, s33
	v_lshl_add_u64 v[194:195], v[194:195], 0, s[56:57]
	s_mov_b32 m0, s28
	ds_read_b128 v[174:177], v184 offset:49152
	ds_read_b128 v[178:181], v184 offset:50176
	ds_read_b128 v[186:189], v184 offset:51200
	ds_read_b128 v[190:193], v184 offset:52224
	ds_read_b128 v[206:209], v184 offset:53248
	ds_read_b128 v[210:213], v184 offset:54272
	ds_read_b128 v[216:219], v184 offset:55296
	ds_read_b128 v[220:223], v184 offset:56320
	global_load_lds_dwordx4 v[194:195], off
	s_add_i32 m0, s28, 0x2000
	s_add_u32 s28, s80, 0x40080
	v_lshl_add_u64 v[194:195], v[224:225], 0, s[56:57]
	s_addc_u32 s29, s81, 0
	s_add_i32 s30, s31, s33
	global_load_lds_dwordx4 v[194:195], off
	v_lshl_add_u64 v[194:195], s[28:29], 0, v[140:141]
	s_mov_b32 m0, s30
	s_nop 0
	global_load_lds_dwordx4 v[194:195], off
	v_lshl_add_u64 v[194:195], s[28:29], 0, v[144:145]
	s_add_i32 m0, s30, 0x2000
	s_nop 0
	global_load_lds_dwordx4 v[194:195], off
	v_lshl_add_u64 v[194:195], v[226:227], 0, s[56:57]
	s_mov_b32 m0, s86
	s_nop 0
	global_load_lds_dwordx4 v[194:195], off
	v_lshl_add_u64 v[194:195], v[228:229], 0, s[56:57]
	s_mov_b32 m0, s96
	s_nop 0
	global_load_lds_dwordx4 v[194:195], off
	s_waitcnt vmcnt(8)
	s_waitcnt lgkmcnt(0)
	s_barrier
	s_setprio 1
	s_waitcnt lgkmcnt(0)
	v_mfma_f32_16x16x32_bf16 v[92:95], v[130:133], v[174:177], v[92:95]
	v_mfma_f32_16x16x32_bf16 v[88:91], v[150:153], v[174:177], v[88:91]
	v_mfma_f32_16x16x32_bf16 v[84:87], v[130:133], v[186:189], v[84:87]
	v_mfma_f32_16x16x32_bf16 v[80:83], v[150:153], v[186:189], v[80:83]
	v_mfma_f32_16x16x32_bf16 v[76:79], v[130:133], v[206:209], v[76:79]
	v_mfma_f32_16x16x32_bf16 v[72:75], v[150:153], v[206:209], v[72:75]
	v_mfma_f32_16x16x32_bf16 v[68:71], v[130:133], v[216:219], v[68:71]
	v_mfma_f32_16x16x32_bf16 v[64:67], v[150:153], v[216:219], v[64:67]
	v_mfma_f32_16x16x32_bf16 v[92:95], v[134:137], v[178:181], v[92:95]
	v_mfma_f32_16x16x32_bf16 v[88:91], v[154:157], v[178:181], v[88:91]
	v_mfma_f32_16x16x32_bf16 v[84:87], v[134:137], v[190:193], v[84:87]
	v_mfma_f32_16x16x32_bf16 v[80:83], v[154:157], v[190:193], v[80:83]
	v_mfma_f32_16x16x32_bf16 v[76:79], v[134:137], v[210:213], v[76:79]
	v_mfma_f32_16x16x32_bf16 v[72:75], v[154:157], v[210:213], v[72:75]
	v_mfma_f32_16x16x32_bf16 v[68:71], v[134:137], v[220:223], v[68:71]
	v_mfma_f32_16x16x32_bf16 v[64:67], v[154:157], v[220:223], v[64:67]
	s_setprio 0
	s_setprio 1
	v_mfma_f32_16x16x32_bf16 v[28:31], v[158:161], v[174:177], v[28:31]
	v_mfma_f32_16x16x32_bf16 v[24:27], v[166:169], v[174:177], v[24:27]
	v_mfma_f32_16x16x32_bf16 v[20:23], v[158:161], v[186:189], v[20:23]
	v_mfma_f32_16x16x32_bf16 v[16:19], v[166:169], v[186:189], v[16:19]
	v_mfma_f32_16x16x32_bf16 v[12:15], v[158:161], v[206:209], v[12:15]
	v_mfma_f32_16x16x32_bf16 v[8:11], v[166:169], v[206:209], v[8:11]
	v_mfma_f32_16x16x32_bf16 v[4:7], v[158:161], v[216:219], v[4:7]
	v_mfma_f32_16x16x32_bf16 v[0:3], v[166:169], v[216:219], v[0:3]
	v_mfma_f32_16x16x32_bf16 v[28:31], v[162:165], v[178:181], v[28:31]
	v_mfma_f32_16x16x32_bf16 v[24:27], v[170:173], v[178:181], v[24:27]
	v_mfma_f32_16x16x32_bf16 v[20:23], v[162:165], v[190:193], v[20:23]
	v_mfma_f32_16x16x32_bf16 v[16:19], v[170:173], v[190:193], v[16:19]
	v_mfma_f32_16x16x32_bf16 v[12:15], v[162:165], v[210:213], v[12:15]
	v_mfma_f32_16x16x32_bf16 v[8:11], v[170:173], v[210:213], v[8:11]
	v_mfma_f32_16x16x32_bf16 v[4:7], v[162:165], v[220:223], v[4:7]
	v_mfma_f32_16x16x32_bf16 v[0:3], v[170:173], v[220:223], v[0:3]
	s_setprio 0
	s_barrier
	s_add_i32 s84, s84, 2
	s_add_u32 s78, s78, 0x100
	s_addc_u32 s79, s79, 0
	s_add_u32 s71, s71, 0x100
	s_addc_u32 s77, s77, 0
	s_cmp_gt_u32 s84, 13

.LBB0_1165:
	s_ashr_i32 s49, s48, 31
	s_lshl_b64 s[30:31], s[48:49], 18
	v_readlane_b32 s44, v254, 30
	v_readlane_b32 s45, v254, 31
	s_add_u32 s70, s44, s30
	s_addc_u32 s71, s45, s31
	s_and_b64 s[30:31], s[50:51], exec
	s_cselect_b32 s27, s71, s73
	s_cselect_b32 s37, s70, s72
	s_add_u32 s72, s72, 0x20080
	s_addc_u32 s73, s73, 0
	s_add_u32 s47, s74, 0x100
	s_addc_u32 s49, s75, 0
	s_mov_b32 s50, -2
.Lpeel_down:
	s_add_u32 s30, s72, 0xfffe0080
	s_addc_u32 s31, s73, -1
	s_add_i32 s51, 0, 0x10000
	s_cmp_eq_u32 s50, 4
	s_cselect_b32 s77, s27, s31
	s_cselect_b32 s76, s37, s30
	s_cselect_b32 s75, s65, s49
	s_cselect_b32 s74, s64, s47
	s_add_i32 s58, 0, 0x14000
	v_add_u32_e32 v0, s51, v183
	v_add_u32_e32 v12, s58, v183
	ds_read_b128 v[16:19], v0
	ds_read_b128 v[20:23], v0 offset:1024
	ds_read_b128 v[24:27], v0 offset:2048
	ds_read_b128 v[28:31], v0 offset:3072
	ds_read_b128 v[0:3], v12
	ds_read_b128 v[4:7], v12 offset:1024
	ds_read_b128 v[8:11], v12 offset:2048
	ds_read_b128 v[12:15], v12 offset:3072
	v_lshl_add_u64 v[194:195], s[72:73], 0, v[168:169]
	s_add_i32 m0, s7, 0xc000
	ds_read_b128 v[174:177], v184
	ds_read_b128 v[178:181], v184 offset:1024
	ds_read_b128 v[186:189], v184 offset:2048
	ds_read_b128 v[190:193], v184 offset:3072
	ds_read_b128 v[206:209], v184 offset:4096
	ds_read_b128 v[210:213], v184 offset:5120
	ds_read_b128 v[216:219], v184 offset:6144
	ds_read_b128 v[220:223], v184 offset:7168
	global_load_lds_dwordx4 v[194:195], off
	v_lshl_add_u64 v[194:195], s[72:73], 0, v[170:171]
	s_add_i32 m0, s7, 0xe000
	s_nop 0
	global_load_lds_dwordx4 v[194:195], off
	s_waitcnt vmcnt(8)
	s_waitcnt lgkmcnt(0)
	s_barrier
	s_setprio 1
	s_waitcnt lgkmcnt(0)
	v_mfma_scale_f32_16x16x128_f8f6f4 v[158:161], v[16:23], v[174:181], 0, v200, v201 op_sel_hi:[0,0,0]
	v_mfma_scale_f32_16x16x128_f8f6f4 v[154:157], v[24:31], v[174:181], 0, v200, v201 op_sel_hi:[0,0,0]
	v_mfma_scale_f32_16x16x128_f8f6f4 v[142:145], v[16:23], v[186:193], 0, v200, v201 op_sel_hi:[0,0,0]
	v_mfma_scale_f32_16x16x128_f8f6f4 v[138:141], v[24:31], v[186:193], 0, v200, v201 op_sel_hi:[0,0,0]
	v_mfma_scale_f32_16x16x128_f8f6f4 v[126:129], v[16:23], v[206:213], 0, v200, v201 op_sel_hi:[0,0,0]
	v_mfma_scale_f32_16x16x128_f8f6f4 v[122:125], v[24:31], v[206:213], 0, v200, v201 op_sel_hi:[0,0,0]
	v_mfma_scale_f32_16x16x128_f8f6f4 v[108:111], v[16:23], v[216:223], 0, v200, v201 op_sel_hi:[0,0,0]
	v_mfma_scale_f32_16x16x128_f8f6f4 v[104:107], v[24:31], v[216:223], 0, v200, v201 op_sel_hi:[0,0,0]
	s_setprio 0
	s_setprio 1
	v_mfma_scale_f32_16x16x128_f8f6f4 v[150:153], v[0:7], v[174:181], 0, v200, v201 op_sel_hi:[0,0,0]
	v_mfma_scale_f32_16x16x128_f8f6f4 v[146:149], v[8:15], v[174:181], 0, v200, v201 op_sel_hi:[0,0,0]
	v_mfma_scale_f32_16x16x128_f8f6f4 v[134:137], v[0:7], v[186:193], 0, v200, v201 op_sel_hi:[0,0,0]
	v_mfma_scale_f32_16x16x128_f8f6f4 v[130:133], v[8:15], v[186:193], 0, v200, v201 op_sel_hi:[0,0,0]
	v_mfma_scale_f32_16x16x128_f8f6f4 v[118:121], v[0:7], v[206:213], 0, v200, v201 op_sel_hi:[0,0,0]
	v_mfma_scale_f32_16x16x128_f8f6f4 v[114:117], v[8:15], v[206:213], 0, v200, v201 op_sel_hi:[0,0,0]
	v_mfma_scale_f32_16x16x128_f8f6f4 v[100:103], v[0:7], v[216:223], 0, v200, v201 op_sel_hi:[0,0,0]
	v_mfma_scale_f32_16x16x128_f8f6f4 v[96:99], v[8:15], v[216:223], 0, v200, v201 op_sel_hi:[0,0,0]
	s_setprio 0
	s_barrier
	s_add_i32 s30, s51, s14
	v_lshl_add_u64 v[174:175], s[74:75], 0, v[112:113]
	s_mov_b32 m0, s30
	ds_read_b128 v[186:189], v184 offset:16384
	ds_read_b128 v[190:193], v184 offset:17408
	ds_read_b128 v[206:209], v184 offset:18432
	ds_read_b128 v[210:213], v184 offset:19456
	ds_read_b128 v[216:219], v184 offset:20480
	ds_read_b128 v[220:223], v184 offset:21504
	ds_read_b128 v[224:227], v184 offset:22528
	ds_read_b128 v[228:231], v184 offset:23552
	global_load_lds_dwordx4 v[174:175], off
	s_add_i32 m0, s30, 0x2000
	s_add_u32 s30, s74, 0x20000
	v_lshl_add_u64 v[176:177], s[74:75], 0, v[162:163]
	s_addc_u32 s31, s75, 0
	s_add_i32 s45, s58, s14
	global_load_lds_dwordx4 v[176:177], off
	v_lshl_add_u64 v[178:179], s[30:31], 0, v[112:113]
	s_mov_b32 m0, s45
	v_lshl_add_u64 v[180:181], s[76:77], 0, v[164:165]
	global_load_lds_dwordx4 v[178:179], off
	v_lshl_add_u64 v[178:179], s[30:31], 0, v[162:163]
	s_add_i32 m0, s45, 0x2000
	s_nop 0
	global_load_lds_dwordx4 v[178:179], off
	v_lshl_add_u64 v[178:179], s[76:77], 0, v[166:167]
	s_mov_b32 m0, s7
	s_nop 0
	global_load_lds_dwordx4 v[178:179], off
	s_mov_b32 m0, s25
	s_nop 0
	global_load_lds_dwordx4 v[180:181], off
	s_waitcnt vmcnt(8)
	s_waitcnt lgkmcnt(0)
	s_barrier
	s_setprio 1
	s_waitcnt lgkmcnt(0)
	v_mfma_scale_f32_16x16x128_f8f6f4 v[92:95], v[16:23], v[186:193], 0, v200, v201 op_sel_hi:[0,0,0]
	v_mfma_scale_f32_16x16x128_f8f6f4 v[88:91], v[24:31], v[186:193], 0, v200, v201 op_sel_hi:[0,0,0]
	v_mfma_scale_f32_16x16x128_f8f6f4 v[76:79], v[16:23], v[206:213], 0, v200, v201 op_sel_hi:[0,0,0]
	v_mfma_scale_f32_16x16x128_f8f6f4 v[72:75], v[24:31], v[206:213], 0, v200, v201 op_sel_hi:[0,0,0]
	v_mfma_scale_f32_16x16x128_f8f6f4 v[60:63], v[16:23], v[216:223], 0, v200, v201 op_sel_hi:[0,0,0]
	v_mfma_scale_f32_16x16x128_f8f6f4 v[56:59], v[24:31], v[216:223], 0, v200, v201 op_sel_hi:[0,0,0]
	v_mfma_scale_f32_16x16x128_f8f6f4 v[44:47], v[16:23], v[224:231], 0, v200, v201 op_sel_hi:[0,0,0]
	v_mfma_scale_f32_16x16x128_f8f6f4 v[40:43], v[24:31], v[224:231], 0, v200, v201 op_sel_hi:[0,0,0]
	s_setprio 0
	s_setprio 1
	v_mfma_scale_f32_16x16x128_f8f6f4 v[84:87], v[0:7], v[186:193], 0, v200, v201 op_sel_hi:[0,0,0]
	v_mfma_scale_f32_16x16x128_f8f6f4 v[80:83], v[8:15], v[186:193], 0, v200, v201 op_sel_hi:[0,0,0]
	v_mfma_scale_f32_16x16x128_f8f6f4 v[68:71], v[0:7], v[206:213], 0, v200, v201 op_sel_hi:[0,0,0]
	v_mfma_scale_f32_16x16x128_f8f6f4 v[64:67], v[8:15], v[206:213], 0, v200, v201 op_sel_hi:[0,0,0]
	v_mfma_scale_f32_16x16x128_f8f6f4 v[52:55], v[0:7], v[216:223], 0, v200, v201 op_sel_hi:[0,0,0]
	v_mfma_scale_f32_16x16x128_f8f6f4 v[48:51], v[8:15], v[216:223], 0, v200, v201 op_sel_hi:[0,0,0]
	v_mfma_scale_f32_16x16x128_f8f6f4 v[36:39], v[0:7], v[224:231], 0, v200, v201 op_sel_hi:[0,0,0]
	v_mfma_scale_f32_16x16x128_f8f6f4 v[32:35], v[8:15], v[224:231], 0, v200, v201 op_sel_hi:[0,0,0]
	s_setprio 0
	s_barrier
	s_add_i32 s45, 0, 0x18000
	s_add_i32 s51, 0, 0x1c000
	v_add_u32_e32 v12, s45, v183
	v_add_u32_e32 v28, s51, v183
	ds_read_b128 v[0:3], v12
	ds_read_b128 v[4:7], v12 offset:1024
	ds_read_b128 v[8:11], v12 offset:2048
	ds_read_b128 v[12:15], v12 offset:3072
	ds_read_b128 v[16:19], v28
	ds_read_b128 v[20:23], v28 offset:1024
	ds_read_b128 v[24:27], v28 offset:2048
	ds_read_b128 v[28:31], v28 offset:3072
	s_add_u32 s30, s76, 0x20000
	s_addc_u32 s31, s77, 0
	s_mov_b32 m0, s33
	v_lshl_add_u64 v[194:195], s[30:31], 0, v[166:167]
	ds_read_b128 v[186:189], v184 offset:32768
	ds_read_b128 v[190:193], v184 offset:33792
	ds_read_b128 v[206:209], v184 offset:34816
	ds_read_b128 v[210:213], v184 offset:35840
	ds_read_b128 v[216:219], v184 offset:36864
	ds_read_b128 v[220:223], v184 offset:37888
	ds_read_b128 v[224:227], v184 offset:38912
	ds_read_b128 v[228:231], v184 offset:39936
	global_load_lds_dwordx4 v[194:195], off
	v_lshl_add_u64 v[194:195], s[30:31], 0, v[164:165]
	s_mov_b32 m0, s34
	s_nop 0
	global_load_lds_dwordx4 v[194:195], off
	s_waitcnt vmcnt(8)
	s_waitcnt lgkmcnt(0)
	s_barrier
	s_setprio 1
	s_waitcnt lgkmcnt(0)
	v_mfma_scale_f32_16x16x128_f8f6f4 v[158:161], v[0:7], v[186:193], v[158:161], v200, v201 op_sel_hi:[0,0,0]
	v_mfma_scale_f32_16x16x128_f8f6f4 v[154:157], v[8:15], v[186:193], v[154:157], v200, v201 op_sel_hi:[0,0,0]
	v_mfma_scale_f32_16x16x128_f8f6f4 v[142:145], v[0:7], v[206:213], v[142:145], v200, v201 op_sel_hi:[0,0,0]
	v_mfma_scale_f32_16x16x128_f8f6f4 v[138:141], v[8:15], v[206:213], v[138:141], v200, v201 op_sel_hi:[0,0,0]
	v_mfma_scale_f32_16x16x128_f8f6f4 v[126:129], v[0:7], v[216:223], v[126:129], v200, v201 op_sel_hi:[0,0,0]
	v_mfma_scale_f32_16x16x128_f8f6f4 v[122:125], v[8:15], v[216:223], v[122:125], v200, v201 op_sel_hi:[0,0,0]
	v_mfma_scale_f32_16x16x128_f8f6f4 v[108:111], v[0:7], v[224:231], v[108:111], v200, v201 op_sel_hi:[0,0,0]
	v_mfma_scale_f32_16x16x128_f8f6f4 v[104:107], v[8:15], v[224:231], v[104:107], v200, v201 op_sel_hi:[0,0,0]
	s_setprio 0
	s_setprio 1
	v_mfma_scale_f32_16x16x128_f8f6f4 v[150:153], v[16:23], v[186:193], v[150:153], v200, v201 op_sel_hi:[0,0,0]
	v_mfma_scale_f32_16x16x128_f8f6f4 v[146:149], v[24:31], v[186:193], v[146:149], v200, v201 op_sel_hi:[0,0,0]
	v_mfma_scale_f32_16x16x128_f8f6f4 v[134:137], v[16:23], v[206:213], v[134:137], v200, v201 op_sel_hi:[0,0,0]
	v_mfma_scale_f32_16x16x128_f8f6f4 v[130:133], v[24:31], v[206:213], v[130:133], v200, v201 op_sel_hi:[0,0,0]
	v_mfma_scale_f32_16x16x128_f8f6f4 v[118:121], v[16:23], v[216:223], v[118:121], v200, v201 op_sel_hi:[0,0,0]
	v_mfma_scale_f32_16x16x128_f8f6f4 v[114:117], v[24:31], v[216:223], v[114:117], v200, v201 op_sel_hi:[0,0,0]
	v_mfma_scale_f32_16x16x128_f8f6f4 v[100:103], v[16:23], v[224:231], v[100:103], v200, v201 op_sel_hi:[0,0,0]
	v_mfma_scale_f32_16x16x128_f8f6f4 v[96:99], v[24:31], v[224:231], v[96:99], v200, v201 op_sel_hi:[0,0,0]
	s_setprio 0
	s_barrier
	s_add_i32 s30, s45, s14
	v_lshl_add_u64 v[174:175], v[174:175], 0, s[56:57]
	s_mov_b32 m0, s30
	ds_read_b128 v[186:189], v184 offset:49152
	ds_read_b128 v[190:193], v184 offset:50176
	ds_read_b128 v[206:209], v184 offset:51200
	ds_read_b128 v[210:213], v184 offset:52224
	ds_read_b128 v[216:219], v184 offset:53248
	ds_read_b128 v[220:223], v184 offset:54272
	ds_read_b128 v[224:227], v184 offset:55296
	ds_read_b128 v[228:231], v184 offset:56320
	global_load_lds_dwordx4 v[174:175], off
	s_add_i32 m0, s30, 0x2000
	s_add_u32 s30, s74, 0x20080
	v_lshl_add_u64 v[174:175], v[176:177], 0, s[56:57]
	s_addc_u32 s31, s75, 0
	s_add_i32 s45, s51, s14
	global_load_lds_dwordx4 v[174:175], off
	v_lshl_add_u64 v[174:175], s[30:31], 0, v[112:113]
	s_mov_b32 m0, s45
	s_nop 0
	global_load_lds_dwordx4 v[174:175], off
	v_lshl_add_u64 v[174:175], s[30:31], 0, v[162:163]
	s_add_i32 m0, s45, 0x2000
	s_nop 0
	global_load_lds_dwordx4 v[174:175], off
	v_lshl_add_u64 v[174:175], v[178:179], 0, s[56:57]
	s_mov_b32 m0, s4
	s_nop 0
	global_load_lds_dwordx4 v[174:175], off
	v_lshl_add_u64 v[174:175], v[180:181], 0, s[56:57]
	s_mov_b32 m0, s54
	s_nop 0
	global_load_lds_dwordx4 v[174:175], off
	s_waitcnt vmcnt(8)
	s_waitcnt lgkmcnt(0)
	s_barrier
	s_setprio 1
	s_waitcnt lgkmcnt(0)
	v_mfma_scale_f32_16x16x128_f8f6f4 v[92:95], v[0:7], v[186:193], v[92:95], v200, v201 op_sel_hi:[0,0,0]
	v_mfma_scale_f32_16x16x128_f8f6f4 v[88:91], v[8:15], v[186:193], v[88:91], v200, v201 op_sel_hi:[0,0,0]
	v_mfma_scale_f32_16x16x128_f8f6f4 v[76:79], v[0:7], v[206:213], v[76:79], v200, v201 op_sel_hi:[0,0,0]
	v_mfma_scale_f32_16x16x128_f8f6f4 v[72:75], v[8:15], v[206:213], v[72:75], v200, v201 op_sel_hi:[0,0,0]
	v_mfma_scale_f32_16x16x128_f8f6f4 v[60:63], v[0:7], v[216:223], v[60:63], v200, v201 op_sel_hi:[0,0,0]
	v_mfma_scale_f32_16x16x128_f8f6f4 v[56:59], v[8:15], v[216:223], v[56:59], v200, v201 op_sel_hi:[0,0,0]
	v_mfma_scale_f32_16x16x128_f8f6f4 v[44:47], v[0:7], v[224:231], v[44:47], v200, v201 op_sel_hi:[0,0,0]
	v_mfma_scale_f32_16x16x128_f8f6f4 v[40:43], v[8:15], v[224:231], v[40:43], v200, v201 op_sel_hi:[0,0,0]
	s_setprio 0
	s_setprio 1
	v_mfma_scale_f32_16x16x128_f8f6f4 v[84:87], v[16:23], v[186:193], v[84:87], v200, v201 op_sel_hi:[0,0,0]
	v_mfma_scale_f32_16x16x128_f8f6f4 v[80:83], v[24:31], v[186:193], v[80:83], v200, v201 op_sel_hi:[0,0,0]
	v_mfma_scale_f32_16x16x128_f8f6f4 v[68:71], v[16:23], v[206:213], v[68:71], v200, v201 op_sel_hi:[0,0,0]
	v_mfma_scale_f32_16x16x128_f8f6f4 v[64:67], v[24:31], v[206:213], v[64:67], v200, v201 op_sel_hi:[0,0,0]
	v_mfma_scale_f32_16x16x128_f8f6f4 v[52:55], v[16:23], v[216:223], v[52:55], v200, v201 op_sel_hi:[0,0,0]
	v_mfma_scale_f32_16x16x128_f8f6f4 v[48:51], v[24:31], v[216:223], v[48:51], v200, v201 op_sel_hi:[0,0,0]
	v_mfma_scale_f32_16x16x128_f8f6f4 v[36:39], v[16:23], v[224:231], v[36:39], v200, v201 op_sel_hi:[0,0,0]
	v_mfma_scale_f32_16x16x128_f8f6f4 v[32:35], v[24:31], v[224:231], v[32:35], v200, v201 op_sel_hi:[0,0,0]
	s_setprio 0
	s_barrier
	s_add_i32 s50, s50, 2
	s_add_u32 s72, s72, 0x100
	s_addc_u32 s73, s73, 0
	s_add_u32 s47, s47, 0x100
	s_addc_u32 s49, s49, 0
	s_cmp_gt_u32 s50, 5
